# deferred weight-conversion split retuned on the combined version: 1900 gate/up + 950 down tiles deferred, idle-slot quotas 5/6/6/6
# baseline (speedup 1.0000x reference)
; __device__ __forceinline__ void bt_load(const float* __restrict__ src, int N, int perm, int it, int ntn, f32x4 (&v)[8]) {
;     const int wid = threadIdx.x >> 6, lane = threadIdx.x & 63;
;     const int per = 16 * ntn, z = it / per, r = it % per, kt = r / ntn, nt = r % ntn;
;     const int np = nt * 256 + lane * 4;
;     const int sc = perm ? (nt * 128 + (lane & 31) * 4 + (lane >> 5) * 1024) : np;
;     const float* p = src + (size_t)z * 1024 * N + (size_t)(kt * 64 + wid * 8) * N + sc;
; #pragma unroll
;     for (int i = 0; i < 8; ++i) v[i] = __builtin_nontemporal_load((const f32x4*)(p + (size_t)i * N));
; }
; __device__ __forceinline__ void ph_big_transpose(const float* __restrict__ src, int N, int perm, int batch, bf16* __restrict__ dst, float* tile  , int G, int ndefer) {
;     const int tid = threadIdx.x, wid = tid >> 6, lane = tid & 63, ntn = N / 256, total = batch * 16 * ntn - ndefer;
;     int it = (int)blockIdx.x;
;     if (it >= total) return;
;     f32x4 cur[8], nxt[8], nx2[8];
;     bt_load(src, N, perm, it, ntn, cur);
;     if (it + G < total) bt_load(src, N, perm, it + G, ntn, nxt);
;     for (; it < total; it += G) {
;         const bool more = it + G < total, more2 = it + 2 * G < total;
;         if (more2) bt_load(src, N, perm, it + 2 * G, ntn, nx2);
.LBB0_63:
	s_cmpk_gt_i32 s2, 0x1893
	s_waitcnt lgkmcnt(0)
	s_barrier
	s_cbranch_scc1 .LBB0_71
	s_ashr_i32 s0, s2, 31
	s_lshr_b32 s0, s0, 25
	s_add_i32 s1, s2, s0
	s_ashr_i32 s0, s1, 7
	s_and_b32 s1, s1, 0xff80
	s_sub_i32 s1, s2, s1
	s_bfe_i32 s4, s1, 0x80000
	s_bfe_u32 s4, s4, 0x3000c
	s_add_i32 s4, s1, s4
	s_bfe_i32 s5, s4, 0x80000
	s_and_b32 s4, s4, 0xf8
	v_lshlrev_b32_e32 v2, 2, v0
	s_sub_i32 s1, s1, s4
	v_and_b32_e32 v2, 0x7c, v2
	v_lshlrev_b32_e32 v3, 5, v0
	s_movk_i32 s4, 0x400
	s_sext_i32_i8 s1, s1
	v_and_or_b32 v99, v3, s4, v2
	v_lshl_add_u32 v2, s1, 7, v99
	s_ashr_i32 s1, s0, 31
	s_lshl_b64 s[0:1], s[0:1], 23
	s_sext_i32_i16 s5, s5
	s_add_u32 s0, s68, s0
	s_addc_u32 s1, s69, s1
	s_lshl_b32 s4, s5, 3
	v_lshrrev_b32_e32 v3, 3, v0
	s_andn2_b32 s4, s4, 63
	v_and_b32_e32 v110, 56, v3
	v_or_b32_e32 v4, s4, v110
	v_ashrrev_i32_e32 v5, 31, v4
	v_lshlrev_b64 v[4:5], 13, v[4:5]
	v_lshl_add_u64 v[4:5], s[0:1], 0, v[4:5]
	v_ashrrev_i32_e32 v3, 31, v2
	v_lshl_add_u64 v[2:3], v[2:3], 2, v[4:5]
	s_movk_i32 s0, 0x2000
	v_add_co_u32_e32 v4, vcc, s0, v2
	s_movk_i32 s1, 0x4000
	s_nop 0
	v_addc_co_u32_e32 v5, vcc, 0, v3, vcc
	global_load_dwordx4 v[38:41], v[2:3], off nt
	global_load_dwordx4 v[34:37], v[4:5], off nt
	v_add_co_u32_e32 v4, vcc, s1, v2
	s_movk_i32 s4, 0x6000
	s_nop 0
	v_addc_co_u32_e32 v5, vcc, 0, v3, vcc
	v_add_co_u32_e32 v6, vcc, s4, v2
	s_mov_b32 s5, 0x8000
	s_nop 0
	v_addc_co_u32_e32 v7, vcc, 0, v3, vcc
	global_load_dwordx4 v[46:49], v[4:5], off nt
	global_load_dwordx4 v[42:45], v[6:7], off nt
	v_add_co_u32_e32 v4, vcc, s5, v2
	s_mov_b32 s6, 0xa000
	s_nop 0
	v_addc_co_u32_e32 v5, vcc, 0, v3, vcc
	v_add_co_u32_e32 v6, vcc, s6, v2
	s_add_i32 s6, s62, s2
	s_nop 0
	v_addc_co_u32_e32 v7, vcc, 0, v3, vcc
	global_load_dwordx4 v[54:57], v[4:5], off nt
	global_load_dwordx4 v[50:53], v[6:7], off nt
	v_add_co_u32_e32 v4, vcc, 0xc000, v2
	s_cmpk_gt_i32 s6, 0x1893
	s_nop 0
	v_addc_co_u32_e32 v5, vcc, 0, v3, vcc
	v_add_co_u32_e32 v2, vcc, 0xe000, v2
	s_nop 1
	v_addc_co_u32_e32 v3, vcc, 0, v3, vcc
	global_load_dwordx4 v[62:65], v[4:5], off nt
	global_load_dwordx4 v[58:61], v[2:3], off nt
	s_cbranch_scc1 .LBB0_66
	s_ashr_i32 s7, s6, 31
	s_lshr_b32 s7, s7, 25
	s_add_i32 s7, s6, s7
	s_ashr_i32 s8, s7, 7
	s_and_b32 s7, s7, 0xff80
	s_sub_i32 s6, s6, s7
	s_bfe_i32 s7, s6, 0x80000
	s_bfe_u32 s7, s7, 0x3000c
	s_add_i32 s7, s6, s7
	s_bfe_i32 s9, s7, 0x80000
	s_and_b32 s7, s7, 0xf8
	s_sub_i32 s6, s6, s7
	s_sext_i32_i16 s10, s9
	s_sext_i32_i8 s6, s6
	s_ashr_i32 s9, s8, 31
	v_lshl_add_u32 v2, s6, 7, v99
	s_lshl_b64 s[6:7], s[8:9], 23
	s_add_u32 s6, s68, s6
	s_addc_u32 s7, s69, s7
	s_lshl_b32 s8, s10, 3
	s_andn2_b32 s8, s8, 63
	v_or_b32_e32 v4, s8, v110
	v_ashrrev_i32_e32 v5, 31, v4
	v_lshlrev_b64 v[4:5], 13, v[4:5]
	v_lshl_add_u64 v[4:5], s[6:7], 0, v[4:5]
	v_ashrrev_i32_e32 v3, 31, v2
	v_lshl_add_u64 v[26:27], v[2:3], 2, v[4:5]
	v_add_co_u32_e32 v6, vcc, s0, v26
	s_nop 1
	v_addc_co_u32_e32 v7, vcc, 0, v27, vcc
	v_add_co_u32_e32 v10, vcc, s1, v26
	global_load_dwordx4 v[2:5], v[26:27], off nt
	s_nop 0
	global_load_dwordx4 v[6:9], v[6:7], off nt
	v_addc_co_u32_e32 v11, vcc, 0, v27, vcc
	v_add_co_u32_e32 v14, vcc, s4, v26
	s_nop 1
	v_addc_co_u32_e32 v15, vcc, 0, v27, vcc
	v_add_co_u32_e32 v18, vcc, s5, v26
	global_load_dwordx4 v[10:13], v[10:11], off nt
	s_nop 0
	global_load_dwordx4 v[14:17], v[14:15], off nt
	v_addc_co_u32_e32 v19, vcc, 0, v27, vcc
	v_add_co_u32_e32 v22, vcc, 0xa000, v26
	s_nop 1
	v_addc_co_u32_e32 v23, vcc, 0, v27, vcc
	v_add_co_u32_e32 v28, vcc, 0xc000, v26
	global_load_dwordx4 v[18:21], v[18:19], off nt
	s_nop 0
	global_load_dwordx4 v[22:25], v[22:23], off nt
	v_addc_co_u32_e32 v29, vcc, 0, v27, vcc
	v_add_co_u32_e32 v30, vcc, 0xe000, v26
	s_nop 1
	v_addc_co_u32_e32 v31, vcc, 0, v27, vcc
	global_load_dwordx4 v[26:29], v[28:29], off nt
	s_nop 0
	global_load_dwordx4 v[30:33], v[30:31], off nt

; __device__ __forceinline__ unsigned g8_cvt_pk(float lo, float hi) { unsigned r; asm volatile("v_cvt_pk_bf16_f32 %0, %1, %2" : "=v"(r) : "v"(lo), "v"(hi)); return r; }
; __device__ __forceinline__ void ph_big_transpose(const float* __restrict__ src, int N, int perm, int batch, bf16* __restrict__ dst, float* tile  , int G, int ndefer) {
;     ...
;     for (; it < total; it += G) {
;         const bool more = it + G < total, more2 = it + 2 * G < total;
;         if (more2) bt_load(src, N, perm, it + 2 * G, ntn, nx2);
;         __syncthreads();
; #pragma unroll
;         for (int i = 0; i < 8; ++i) { float* t = tile + (wid * 8 + i) * 257 + lane * 4; t[0] = cur[i][0]; t[1] = cur[i][1]; t[2] = cur[i][2]; t[3] = cur[i][3]; }
;         __syncthreads();
;         const int per = 16 * ntn, z = it / per, r = it % per, kt = r / ntn, nt = r % ntn;
;         bf16* d = dst + (size_t)z * N * 1024 + (((size_t)nt * 16 + kt) << 14);
;         const int kc = lane & 7;
; #pragma unroll
;         for (int pss = 0; pss < 4; ++pss) {
;             const int n = wid * 32 + pss * 8 + (lane >> 3); float f[8];
; #pragma unroll
;             for (int j = 0; j < 8; ++j) f[j] = tile[(kc * 8 + j) * 257 + n];
;             u32x4 w; w.x = g8_cvt_pk(f[0], f[1]); w.y = g8_cvt_pk(f[2], f[3]); w.z = g8_cvt_pk(f[4], f[5]); w.w = g8_cvt_pk(f[6], f[7]);
;             __builtin_nontemporal_store(w, (u32x4*)(d + n * 64 + kc * 8));
;         }
;         if (more) {
; #pragma unroll
;             for (int i = 0; i < 8; ++i) { cur[i] = nxt[i]; nxt[i] = nx2[i]; } }
.LBB0_67:
	s_barrier
	s_waitcnt vmcnt(7)
	ds_write_b128 v111, v[38:41]
	v_add_u32_e32 v38, 0x404, v111
	s_ashr_i32 s9, s8, 31
	s_waitcnt vmcnt(6)
	ds_write2_b32 v38, v34, v35 offset1:1
	v_add_u32_e32 v34, 0x40c, v111
	s_lshr_b32 s9, s9, 25
	ds_write2_b32 v34, v36, v37 offset1:1
	v_add_u32_e32 v34, 0x808, v111
	s_add_i32 s9, s8, s9
	s_waitcnt vmcnt(5)
	ds_write2_b64 v34, v[46:47], v[48:49] offset1:1
	v_add_u32_e32 v34, 0xc0c, v111
	s_ashr_i32 s10, s9, 7
	s_and_b32 s9, s9, 0xff80
	s_waitcnt vmcnt(4)
	ds_write2_b32 v34, v42, v43 offset1:1
	v_add_u32_e32 v34, 0xc14, v111
	s_sub_i32 s9, s8, s9
	s_add_i32 s31, s8, s62
	ds_write2_b32 v34, v44, v45 offset1:1
	s_waitcnt vmcnt(3)
	ds_write_b128 v111, v[54:57] offset:4112
	v_add_u32_e32 v34, 0x1414, v111
	s_bfe_i32 s8, s9, 0x80000
	s_waitcnt vmcnt(2)
	ds_write2_b32 v34, v50, v51 offset1:1
	v_add_u32_e32 v34, 0x141c, v111
	s_bfe_u32 s8, s8, 0x3000c
	ds_write2_b32 v34, v52, v53 offset1:1
	v_add_u32_e32 v34, 0x1818, v111
	s_add_i32 s11, s9, s8
	s_waitcnt vmcnt(1)
	ds_write2_b64 v34, v[62:63], v[64:65] offset1:1
	v_add_u32_e32 v34, 0x1c1c, v111
	s_bfe_i32 s8, s11, 0x80000
	s_and_b32 s11, s11, 0xf8
	s_waitcnt vmcnt(0)
	ds_write2_b32 v34, v58, v59 offset1:1
	v_add_u32_e32 v34, 0x1c24, v111
	s_sext_i32_i16 s8, s8
	s_sub_i32 s30, s9, s11
	s_ashr_i32 s11, s10, 31
	ds_write2_b32 v34, v60, v61 offset1:1
	s_waitcnt lgkmcnt(0)
	s_barrier
	s_lshr_b32 s8, s8, 3
	s_lshl_b64 s[10:11], s[10:11], 22
	ds_read_b32 v34, v112 offset:1028
	ds_read_b32 v35, v112 offset:3084
	ds_read_b32 v36, v112 offset:5140
	ds_read_b32 v37, v112 offset:7196
	ds_read_b32 v38, v112 offset:6168
	ds_read_b32 v39, v112 offset:4112
	ds_read_b32 v40, v112 offset:2056
	ds_read_b32 v41, v112
	s_add_u32 s33, s5, s10
	s_addc_u32 s34, s6, s11
	s_bfe_i64 s[10:11], s[30:31], 0x80000
	s_bfe_i64 s[8:9], s[8:9], 0x100000
	s_lshl_b64 s[10:11], s[10:11], 19
	s_add_u32 s10, s33, s10
	s_addc_u32 s11, s34, s11
	s_lshl_b64 s[8:9], s[8:9], 15
	s_waitcnt lgkmcnt(0)
	v_cvt_pk_bf16_f32 v34, v41, v34
	v_cvt_pk_bf16_f32 v35, v40, v35
	v_cvt_pk_bf16_f32 v36, v39, v36
	v_cvt_pk_bf16_f32 v37, v38, v37
	ds_read_b32 v42, v112 offset:1060
	ds_read_b32 v43, v112 offset:3116
	ds_read_b32 v44, v112 offset:5172
	ds_read_b32 v45, v112 offset:7228
	ds_read_b32 v46, v112 offset:6200
	ds_read_b32 v47, v112 offset:4144
	ds_read_b32 v48, v112 offset:2088
	ds_read_b32 v49, v112 offset:32
	s_add_u32 s8, s10, s8
	s_addc_u32 s9, s11, s9
	v_lshl_add_u64 v[38:39], s[8:9], 0, v[100:101]
	v_mov_b32_e32 v103, v101
	v_lshl_add_u64 v[40:41], v[38:39], 0, v[102:103]
	global_store_dwordx4 v[40:41], v[34:37], off nt
	v_mov_b32_e32 v105, v101
	v_lshl_add_u64 v[40:41], v[38:39], 0, v[104:105]
	s_waitcnt lgkmcnt(0)
	v_cvt_pk_bf16_f32 v34, v49, v42
	v_cvt_pk_bf16_f32 v35, v48, v43
	v_cvt_pk_bf16_f32 v36, v47, v44
	v_cvt_pk_bf16_f32 v37, v46, v45
	ds_read_b32 v42, v112 offset:1092
	ds_read_b32 v43, v112 offset:3148
	ds_read_b32 v44, v112 offset:5204
	ds_read_b32 v45, v112 offset:6232
	ds_read_b32 v46, v112 offset:4176
	ds_read_b32 v47, v112 offset:2120
	ds_read_b32 v48, v112 offset:64
	ds_read_b32 v49, v112 offset:7260
	global_store_dwordx4 v[40:41], v[34:37], off nt
	v_mov_b32_e32 v107, v101
	v_lshl_add_u64 v[40:41], v[38:39], 0, v[106:107]
	s_waitcnt lgkmcnt(1)
	v_cvt_pk_bf16_f32 v34, v48, v42
	v_cvt_pk_bf16_f32 v35, v47, v43
	v_cvt_pk_bf16_f32 v36, v46, v44
	s_waitcnt lgkmcnt(0)
	v_cvt_pk_bf16_f32 v37, v45, v49
	ds_read_b32 v42, v112 offset:1124
	ds_read_b32 v43, v112 offset:3180
	ds_read_b32 v44, v112 offset:5236
	ds_read_b32 v45, v112 offset:6264
	ds_read_b32 v46, v112 offset:4208
	ds_read_b32 v47, v112 offset:2152
	ds_read_b32 v48, v112 offset:96
	ds_read_b32 v49, v112 offset:7292
	v_mov_b32_e32 v109, v101
	global_store_dwordx4 v[40:41], v[34:37], off nt
	v_lshl_add_u64 v[38:39], v[38:39], 0, v[108:109]
	v_mov_b64_e32 v[60:61], v[32:33]
	s_waitcnt lgkmcnt(1)
	v_cvt_pk_bf16_f32 v34, v48, v42
	v_cvt_pk_bf16_f32 v35, v47, v43
	v_cvt_pk_bf16_f32 v36, v46, v44
	s_waitcnt lgkmcnt(0)
	v_cvt_pk_bf16_f32 v37, v45, v49
	global_store_dwordx4 v[38:39], v[34:37], off nt
	v_mov_b64_e32 v[64:65], v[28:29]
	v_mov_b64_e32 v[52:53], v[24:25]
	v_mov_b64_e32 v[56:57], v[20:21]
	v_mov_b64_e32 v[44:45], v[16:17]
	v_mov_b64_e32 v[48:49], v[12:13]
	v_mov_b64_e32 v[36:37], v[8:9]
	v_mov_b64_e32 v[40:41], v[4:5]
	v_mov_b64_e32 v[58:59], v[30:31]
	v_mov_b64_e32 v[62:63], v[26:27]
	v_mov_b64_e32 v[50:51], v[22:23]
	v_mov_b64_e32 v[54:55], v[18:19]
	v_mov_b64_e32 v[42:43], v[14:15]
	v_mov_b64_e32 v[46:47], v[10:11]
	v_mov_b64_e32 v[34:35], v[6:7]
	v_mov_b64_e32 v[38:39], v[2:3]
	v_mov_b64_e32 v[30:31], v[94:95]
	v_mov_b64_e32 v[26:27], v[90:91]
	v_mov_b64_e32 v[22:23], v[86:87]
	v_mov_b64_e32 v[18:19], v[82:83]
	v_mov_b64_e32 v[14:15], v[78:79]
	v_mov_b64_e32 v[10:11], v[74:75]
	v_mov_b64_e32 v[6:7], v[70:71]
	v_mov_b64_e32 v[2:3], v[66:67]
	s_cmpk_lt_i32 s31, 0x1894
	v_mov_b64_e32 v[32:33], v[96:97]
	v_mov_b64_e32 v[28:29], v[92:93]
	v_mov_b64_e32 v[24:25], v[88:89]
	v_mov_b64_e32 v[20:21], v[84:85]
	v_mov_b64_e32 v[16:17], v[80:81]
	v_mov_b64_e32 v[12:13], v[76:77]
	v_mov_b64_e32 v[8:9], v[72:73]
	v_mov_b64_e32 v[4:5], v[68:69]
	s_mov_b32 s8, s31
	s_cbranch_scc0 .LBB0_70
; __device__ __forceinline__ void bt_load(const float* __restrict__ src, int N, int perm, int it, int ntn, f32x4 (&v)[8]) {
;     const int wid = threadIdx.x >> 6, lane = threadIdx.x & 63;
;     const int per = 16 * ntn, z = it / per, r = it % per, kt = r / ntn, nt = r % ntn;
;     const int np = nt * 256 + lane * 4;
;     const int sc = perm ? (nt * 128 + (lane & 31) * 4 + (lane >> 5) * 1024) : np;
;     const float* p = src + (size_t)z * 1024 * N + (size_t)(kt * 64 + wid * 8) * N + sc;
; #pragma unroll
;     for (int i = 0; i < 8; ++i) v[i] = __builtin_nontemporal_load((const f32x4*)(p + (size_t)i * N));
; }
; __device__ __forceinline__ void ph_big_transpose(const float* __restrict__ src, int N, int perm, int batch, bf16* __restrict__ dst, float* tile  , int G, int ndefer) {
;     ...
;         const bool more = it + G < total, more2 = it + 2 * G < total;
;         if (more2) bt_load(src, N, perm, it + 2 * G, ntn, nx2);
.LBB0_68:
	s_add_i32 s9, s7, s8
	s_cmpk_gt_i32 s9, 0x1893
	s_cbranch_scc1 .LBB0_67
	s_ashr_i32 s10, s9, 31
	s_lshr_b32 s10, s10, 25
	s_add_i32 s11, s9, s10
	s_ashr_i32 s10, s11, 7
	s_and_b32 s11, s11, 0xff80
	s_sub_i32 s9, s9, s11
	s_bfe_i32 s11, s9, 0x80000
	s_bfe_u32 s11, s11, 0x3000c
	s_add_i32 s11, s9, s11
	s_bfe_i32 s30, s11, 0x80000
	s_and_b32 s11, s11, 0xf8
	s_sub_i32 s9, s9, s11
	s_ashr_i32 s11, s10, 31
	s_lshl_b64 s[10:11], s[10:11], 23
	s_sext_i32_i16 s30, s30
	s_sext_i32_i8 s9, s9
	s_add_u32 s10, s68, s10
	v_lshl_add_u32 v66, s9, 7, v99
	s_addc_u32 s11, s69, s11
	s_lshl_b32 s9, s30, 3
	s_andn2_b32 s9, s9, 63
	v_or_b32_e32 v68, s9, v110
	v_ashrrev_i32_e32 v69, 31, v68
	v_lshlrev_b64 v[68:69], 13, v[68:69]
	v_lshl_add_u64 v[68:69], s[10:11], 0, v[68:69]
	v_ashrrev_i32_e32 v67, 31, v66
	v_lshl_add_u64 v[90:91], v[66:67], 2, v[68:69]
	v_add_co_u32_e32 v70, vcc, s0, v90
	s_nop 1
	v_addc_co_u32_e32 v71, vcc, 0, v91, vcc
	v_add_co_u32_e32 v74, vcc, s1, v90
	global_load_dwordx4 v[66:69], v[90:91], off nt
	s_nop 0
	global_load_dwordx4 v[70:73], v[70:71], off nt
	v_addc_co_u32_e32 v75, vcc, 0, v91, vcc
	v_add_co_u32_e32 v78, vcc, s4, v90
	s_nop 1
	v_addc_co_u32_e32 v79, vcc, 0, v91, vcc
	v_add_co_u32_e32 v82, vcc, 0x8000, v90
	global_load_dwordx4 v[74:77], v[74:75], off nt
	s_nop 0
	global_load_dwordx4 v[78:81], v[78:79], off nt
	v_addc_co_u32_e32 v83, vcc, 0, v91, vcc
	v_add_co_u32_e32 v86, vcc, 0xa000, v90
	s_nop 1
	v_addc_co_u32_e32 v87, vcc, 0, v91, vcc
	v_add_co_u32_e32 v92, vcc, 0xc000, v90
	global_load_dwordx4 v[82:85], v[82:83], off nt
	s_nop 0
	global_load_dwordx4 v[86:89], v[86:87], off nt
	v_addc_co_u32_e32 v93, vcc, 0, v91, vcc
	v_add_co_u32_e32 v94, vcc, 0xe000, v90
	s_nop 1
	v_addc_co_u32_e32 v95, vcc, 0, v91, vcc
	global_load_dwordx4 v[90:93], v[92:93], off nt
	s_nop 0
	global_load_dwordx4 v[94:97], v[94:95], off nt
	s_branch .LBB0_67

; __device__ __forceinline__ void bt_load(const float* __restrict__ src, int N, int perm, int it, int ntn, f32x4 (&v)[8]) {
;     const int wid = threadIdx.x >> 6, lane = threadIdx.x & 63;
;     const int per = 16 * ntn, z = it / per, r = it % per, kt = r / ntn, nt = r % ntn;
;     const int np = nt * 256 + lane * 4;
;     const int sc = perm ? (nt * 128 + (lane & 31) * 4 + (lane >> 5) * 1024) : np;
;     const float* p = src + (size_t)z * 1024 * N + (size_t)(kt * 64 + wid * 8) * N + sc;
; #pragma unroll
;     for (int i = 0; i < 8; ++i) v[i] = __builtin_nontemporal_load((const f32x4*)(p + (size_t)i * N));
; }
; __device__ __forceinline__ void ph_big_transpose(const float* __restrict__ src, int N, int perm, int batch, bf16* __restrict__ dst, float* tile  , int G, int ndefer) {
;     const int tid = threadIdx.x, wid = tid >> 6, lane = tid & 63, ntn = N / 256, total = batch * 16 * ntn - ndefer;
;     int it = (int)blockIdx.x;
;     if (it >= total) return;
;     f32x4 cur[8], nxt[8], nx2[8];
;     bt_load(src, N, perm, it, ntn, cur);
;     if (it + G < total) bt_load(src, N, perm, it + G, ntn, nxt);
;     for (; it < total; it += G) {
;         const bool more = it + G < total, more2 = it + 2 * G < total;
;         if (more2) bt_load(src, N, perm, it + 2 * G, ntn, nx2);
.LBB0_71:
	s_cmpk_gt_i32 s2, 0xc49
	s_cbranch_scc1 .LBB0_79
	s_ashr_i32 s0, s2, 31
	s_lshr_b32 s0, s0, 26
	s_add_i32 s1, s2, s0
	s_ashr_i32 s0, s1, 6
	s_and_b32 s1, s1, 0xffc0
	s_sub_i32 s1, s2, s1
	s_bfe_i32 s4, s1, 0x80000
	s_bfe_u32 s4, s4, 0x2000d
	s_add_i32 s4, s1, s4
	s_bfe_i32 s5, s4, 0x80000
	s_and_b32 s4, s4, 0xfc
	s_sub_i32 s1, s1, s4
	v_lshlrev_b32_e32 v2, 2, v0
	s_sext_i32_i8 s1, s1
	v_and_b32_e32 v99, 0xfc, v2
	v_lshl_or_b32 v2, s1, 8, v99
	s_ashr_i32 s1, s0, 31
	s_lshl_b64 s[0:1], s[0:1], 22
	s_sext_i32_i16 s5, s5
	s_add_u32 s0, s72, s0
	s_addc_u32 s1, s73, s1
	s_lshl_b32 s4, s5, 4
	v_lshrrev_b32_e32 v3, 3, v0
	s_andn2_b32 s4, s4, 63
	v_and_b32_e32 v110, 56, v3
	v_or_b32_e32 v4, s4, v110
	v_ashrrev_i32_e32 v5, 31, v4
	v_lshlrev_b64 v[4:5], 12, v[4:5]
	v_lshl_add_u64 v[4:5], s[0:1], 0, v[4:5]
	v_ashrrev_i32_e32 v3, 31, v2
	v_lshl_add_u64 v[2:3], v[2:3], 2, v[4:5]
	s_movk_i32 s0, 0x2000
	v_add_co_u32_e32 v4, vcc, s0, v2
	s_movk_i32 s4, 0x4000
	s_nop 0
	v_addc_co_u32_e32 v5, vcc, 0, v3, vcc
	global_load_dwordx4 v[42:45], v[4:5], off offset:-4096 nt
	global_load_dwordx4 v[34:37], v[4:5], off nt
	v_add_co_u32_e32 v4, vcc, s4, v2
	s_movk_i32 s1, 0x5000
	s_nop 0
	v_addc_co_u32_e32 v5, vcc, 0, v3, vcc
	global_load_dwordx4 v[46:49], v[4:5], off offset:-4096 nt
	global_load_dwordx4 v[38:41], v[4:5], off nt
	v_add_co_u32_e32 v4, vcc, s1, v2
	s_add_i32 s5, s62, s2
	s_nop 0
	v_addc_co_u32_e32 v5, vcc, 0, v3, vcc
	global_load_dwordx4 v[62:65], v[2:3], off nt
	global_load_dwordx4 v[50:53], v[4:5], off nt
	v_add_co_u32_e32 v4, vcc, 0x6000, v2
	s_cmpk_gt_i32 s5, 0xc49
	s_nop 0
	v_addc_co_u32_e32 v5, vcc, 0, v3, vcc
	v_add_co_u32_e32 v2, vcc, 0x7000, v2
	s_movk_i32 s1, 0x3000
	s_nop 0
	v_addc_co_u32_e32 v3, vcc, 0, v3, vcc
	global_load_dwordx4 v[58:61], v[4:5], off nt
	global_load_dwordx4 v[54:57], v[2:3], off nt
	s_cbranch_scc1 .LBB0_74
	s_ashr_i32 s6, s5, 31
	s_lshr_b32 s6, s6, 26
	s_add_i32 s7, s5, s6
	s_ashr_i32 s6, s7, 6
	s_and_b32 s7, s7, 0xffc0
	s_sub_i32 s5, s5, s7
	s_bfe_i32 s7, s5, 0x80000
	s_bfe_u32 s7, s7, 0x2000d
	s_add_i32 s7, s5, s7
	s_bfe_i32 s8, s7, 0x80000
	s_and_b32 s7, s7, 0xfc
	s_sub_i32 s5, s5, s7
	s_ashr_i32 s7, s6, 31
	s_lshl_b64 s[6:7], s[6:7], 22
	s_sext_i32_i16 s8, s8
	s_sext_i32_i8 s5, s5
	s_add_u32 s6, s72, s6
	v_lshl_or_b32 v2, s5, 8, v99
	s_addc_u32 s7, s73, s7
	s_lshl_b32 s5, s8, 4
	s_andn2_b32 s5, s5, 63
	v_or_b32_e32 v4, s5, v110
	v_ashrrev_i32_e32 v5, 31, v4
	v_lshlrev_b64 v[4:5], 12, v[4:5]
	v_lshl_add_u64 v[4:5], s[6:7], 0, v[4:5]
	v_ashrrev_i32_e32 v3, 31, v2
	v_lshl_add_u64 v[26:27], v[2:3], 2, v[4:5]
	v_add_co_u32_e32 v2, vcc, s0, v26
	s_nop 1
	v_addc_co_u32_e32 v3, vcc, 0, v27, vcc
	v_add_co_u32_e32 v10, vcc, s4, v26
	global_load_dwordx4 v[6:9], v[2:3], off offset:-4096 nt
	s_nop 0
	global_load_dwordx4 v[2:5], v[2:3], off nt
	v_addc_co_u32_e32 v11, vcc, 0, v27, vcc
	v_add_co_u32_e32 v18, vcc, 0x5000, v26
	global_load_dwordx4 v[14:17], v[10:11], off offset:-4096 nt
	s_nop 0
	global_load_dwordx4 v[10:13], v[10:11], off nt
	v_addc_co_u32_e32 v19, vcc, 0, v27, vcc
	v_add_co_u32_e32 v28, vcc, 0x6000, v26
	global_load_dwordx4 v[22:25], v[26:27], off nt
	s_nop 0
	global_load_dwordx4 v[18:21], v[18:19], off nt
	v_addc_co_u32_e32 v29, vcc, 0, v27, vcc
	v_add_co_u32_e32 v30, vcc, 0x7000, v26
	s_nop 1
	v_addc_co_u32_e32 v31, vcc, 0, v27, vcc
	global_load_dwordx4 v[26:29], v[28:29], off nt
	s_nop 0
	global_load_dwordx4 v[30:33], v[30:31], off nt

; __device__ __forceinline__ unsigned g8_cvt_pk(float lo, float hi) { unsigned r; asm volatile("v_cvt_pk_bf16_f32 %0, %1, %2" : "=v"(r) : "v"(lo), "v"(hi)); return r; }
; __device__ __forceinline__ void ph_big_transpose(const float* __restrict__ src, int N, int perm, int batch, bf16* __restrict__ dst, float* tile  , int G, int ndefer) {
;     ...
;     for (; it < total; it += G) {
;         const bool more = it + G < total, more2 = it + 2 * G < total;
;         if (more2) bt_load(src, N, perm, it + 2 * G, ntn, nx2);
;         __syncthreads();
; #pragma unroll
;         for (int i = 0; i < 8; ++i) { float* t = tile + (wid * 8 + i) * 257 + lane * 4; t[0] = cur[i][0]; t[1] = cur[i][1]; t[2] = cur[i][2]; t[3] = cur[i][3]; }
;         __syncthreads();
;         const int per = 16 * ntn, z = it / per, r = it % per, kt = r / ntn, nt = r % ntn;
;         bf16* d = dst + (size_t)z * N * 1024 + (((size_t)nt * 16 + kt) << 14);
;         const int kc = lane & 7;
; #pragma unroll
;         for (int pss = 0; pss < 4; ++pss) {
;             const int n = wid * 32 + pss * 8 + (lane >> 3); float f[8];
; #pragma unroll
;             for (int j = 0; j < 8; ++j) f[j] = tile[(kc * 8 + j) * 257 + n];
;             u32x4 w; w.x = g8_cvt_pk(f[0], f[1]); w.y = g8_cvt_pk(f[2], f[3]); w.z = g8_cvt_pk(f[4], f[5]); w.w = g8_cvt_pk(f[6], f[7]);
;             __builtin_nontemporal_store(w, (u32x4*)(d + n * 64 + kc * 8));
;         }
;         if (more) {
; #pragma unroll
;             for (int i = 0; i < 8; ++i) { cur[i] = nxt[i]; nxt[i] = nx2[i]; } }
.LBB0_75:
	s_ashr_i32 s8, s3, 31
	s_barrier
	s_waitcnt vmcnt(3)
	ds_write_b128 v111, v[62:65]
	v_add_u32_e32 v62, 0x404, v111
	s_lshr_b32 s8, s8, 26
	ds_write2_b32 v62, v42, v43 offset1:1
	v_add_u32_e32 v42, 0x40c, v111
	s_add_i32 s9, s3, s8
	ds_write2_b32 v42, v44, v45 offset1:1
	v_add_u32_e32 v42, 0x808, v111
	s_ashr_i32 s8, s9, 6
	s_and_b32 s9, s9, 0xffc0
	s_add_i32 s7, s3, s62
	ds_write2_b64 v42, v[34:35], v[36:37] offset1:1
	v_add_u32_e32 v34, 0xc0c, v111
	s_sub_i32 s3, s3, s9
	ds_write2_b32 v34, v46, v47 offset1:1
	v_add_u32_e32 v34, 0xc14, v111
	s_bfe_i32 s9, s3, 0x80000
	ds_write2_b32 v34, v48, v49 offset1:1
	ds_write_b128 v111, v[38:41] offset:4112
	v_add_u32_e32 v34, 0x1414, v111
	s_bfe_u32 s9, s9, 0x2000d
	s_waitcnt vmcnt(2)
	ds_write2_b32 v34, v50, v51 offset1:1
	v_add_u32_e32 v34, 0x141c, v111
	s_add_i32 s9, s3, s9
	ds_write2_b32 v34, v52, v53 offset1:1
	v_add_u32_e32 v34, 0x1818, v111
	s_bfe_i32 s10, s9, 0x80000
	s_and_b32 s9, s9, 0xfc
	s_waitcnt vmcnt(1)
	ds_write2_b64 v34, v[58:59], v[60:61] offset1:1
	v_add_u32_e32 v34, 0x1c1c, v111
	s_sext_i32_i16 s10, s10
	s_sub_i32 s30, s3, s9
	s_ashr_i32 s9, s8, 31
	s_waitcnt vmcnt(0)
	ds_write2_b32 v34, v54, v55 offset1:1
	v_add_u32_e32 v34, 0x1c24, v111
	s_lshr_b32 s10, s10, 2
	s_lshl_b64 s[8:9], s[8:9], 21
	ds_write2_b32 v34, v56, v57 offset1:1
	s_waitcnt lgkmcnt(0)
	s_barrier
	s_add_u32 s3, s4, s8
	ds_read_b32 v34, v112 offset:1028
	ds_read_b32 v35, v112 offset:3084
	ds_read_b32 v36, v112 offset:5140
	ds_read_b32 v37, v112 offset:7196
	ds_read_b32 v38, v112 offset:6168
	ds_read_b32 v39, v112 offset:4112
	ds_read_b32 v40, v112 offset:2056
	ds_read_b32 v41, v112
	s_addc_u32 s31, s5, s9
	s_bfe_i64 s[8:9], s[30:31], 0x80000
	s_bfe_i64 s[10:11], s[10:11], 0x100000
	s_lshl_b64 s[8:9], s[8:9], 19
	s_add_u32 s3, s3, s8
	s_addc_u32 s30, s31, s9
	s_lshl_b64 s[8:9], s[10:11], 15
	s_waitcnt lgkmcnt(0)
	v_cvt_pk_bf16_f32 v34, v41, v34
	v_cvt_pk_bf16_f32 v35, v40, v35
	v_cvt_pk_bf16_f32 v36, v39, v36
	v_cvt_pk_bf16_f32 v37, v38, v37
	ds_read_b32 v42, v112 offset:1060
	ds_read_b32 v43, v112 offset:3116
	ds_read_b32 v44, v112 offset:5172
	ds_read_b32 v45, v112 offset:7228
	ds_read_b32 v46, v112 offset:6200
	ds_read_b32 v47, v112 offset:4144
	ds_read_b32 v48, v112 offset:2088
	ds_read_b32 v49, v112 offset:32
	s_add_u32 s8, s3, s8
	s_addc_u32 s9, s30, s9
	v_lshl_add_u64 v[38:39], s[8:9], 0, v[100:101]
	v_mov_b32_e32 v103, v101
	v_lshl_add_u64 v[40:41], v[38:39], 0, v[102:103]
	global_store_dwordx4 v[40:41], v[34:37], off nt
	v_mov_b32_e32 v105, v101
	v_lshl_add_u64 v[40:41], v[38:39], 0, v[104:105]
	s_waitcnt lgkmcnt(0)
	v_cvt_pk_bf16_f32 v34, v49, v42
	v_cvt_pk_bf16_f32 v35, v48, v43
	v_cvt_pk_bf16_f32 v36, v47, v44
	v_cvt_pk_bf16_f32 v37, v46, v45
	ds_read_b32 v42, v112 offset:1092
	ds_read_b32 v43, v112 offset:3148
	ds_read_b32 v44, v112 offset:5204
	ds_read_b32 v45, v112 offset:6232
	ds_read_b32 v46, v112 offset:4176
	ds_read_b32 v47, v112 offset:2120
	ds_read_b32 v48, v112 offset:64
	ds_read_b32 v49, v112 offset:7260
	global_store_dwordx4 v[40:41], v[34:37], off nt
	v_mov_b32_e32 v107, v101
	v_lshl_add_u64 v[40:41], v[38:39], 0, v[106:107]
	s_waitcnt lgkmcnt(1)
	v_cvt_pk_bf16_f32 v34, v48, v42
	v_cvt_pk_bf16_f32 v35, v47, v43
	v_cvt_pk_bf16_f32 v36, v46, v44
	s_waitcnt lgkmcnt(0)
	v_cvt_pk_bf16_f32 v37, v45, v49
	ds_read_b32 v42, v112 offset:1124
	ds_read_b32 v43, v112 offset:3180
	ds_read_b32 v44, v112 offset:5236
	ds_read_b32 v45, v112 offset:6264
	ds_read_b32 v46, v112 offset:4208
	ds_read_b32 v47, v112 offset:2152
	ds_read_b32 v48, v112 offset:96
	ds_read_b32 v49, v112 offset:7292
	v_mov_b32_e32 v109, v101
	global_store_dwordx4 v[40:41], v[34:37], off nt
	v_lshl_add_u64 v[38:39], v[38:39], 0, v[108:109]
	v_mov_b64_e32 v[56:57], v[32:33]
	s_waitcnt lgkmcnt(1)
	v_cvt_pk_bf16_f32 v34, v48, v42
	v_cvt_pk_bf16_f32 v35, v47, v43
	v_cvt_pk_bf16_f32 v36, v46, v44
	s_waitcnt lgkmcnt(0)
	v_cvt_pk_bf16_f32 v37, v45, v49
	global_store_dwordx4 v[38:39], v[34:37], off nt
	v_mov_b64_e32 v[60:61], v[28:29]
	v_mov_b64_e32 v[52:53], v[20:21]
	v_mov_b64_e32 v[40:41], v[12:13]
	v_mov_b64_e32 v[48:49], v[16:17]
	v_mov_b64_e32 v[36:37], v[4:5]
	v_mov_b64_e32 v[44:45], v[8:9]
	v_mov_b64_e32 v[64:65], v[24:25]
	v_mov_b64_e32 v[54:55], v[30:31]
	v_mov_b64_e32 v[58:59], v[26:27]
	v_mov_b64_e32 v[50:51], v[18:19]
	v_mov_b64_e32 v[38:39], v[10:11]
	v_mov_b64_e32 v[46:47], v[14:15]
	v_mov_b64_e32 v[34:35], v[2:3]
	v_mov_b64_e32 v[42:43], v[6:7]
	v_mov_b64_e32 v[62:63], v[22:23]
	v_mov_b64_e32 v[30:31], v[94:95]
	v_mov_b64_e32 v[26:27], v[90:91]
	v_mov_b64_e32 v[18:19], v[86:87]
	v_mov_b64_e32 v[10:11], v[82:83]
	v_mov_b64_e32 v[14:15], v[74:75]
	v_mov_b64_e32 v[2:3], v[66:67]
	v_mov_b64_e32 v[6:7], v[70:71]
	v_mov_b64_e32 v[22:23], v[78:79]
	s_cmpk_lt_i32 s7, 0xc4a
	v_mov_b64_e32 v[32:33], v[96:97]
	v_mov_b64_e32 v[28:29], v[92:93]
	v_mov_b64_e32 v[20:21], v[88:89]
	v_mov_b64_e32 v[12:13], v[84:85]
	v_mov_b64_e32 v[16:17], v[76:77]
	v_mov_b64_e32 v[4:5], v[68:69]
	v_mov_b64_e32 v[8:9], v[72:73]
	v_mov_b64_e32 v[24:25], v[80:81]
	s_mov_b32 s3, s7
	s_cbranch_scc0 .LBB0_78
.LBB0_76:
	s_add_i32 s7, s6, s3
	s_cmpk_gt_i32 s7, 0xc49
	s_cbranch_scc1 .LBB0_75
	s_ashr_i32 s8, s7, 31
	s_lshr_b32 s8, s8, 26
	s_add_i32 s9, s7, s8
	s_ashr_i32 s8, s9, 6
	s_and_b32 s9, s9, 0xffc0
	s_sub_i32 s7, s7, s9
	s_bfe_i32 s9, s7, 0x80000
	s_bfe_u32 s9, s9, 0x2000d
	s_add_i32 s9, s7, s9
	s_bfe_i32 s10, s9, 0x80000
	s_and_b32 s9, s9, 0xfc
	s_sub_i32 s7, s7, s9
	s_ashr_i32 s9, s8, 31
	s_lshl_b64 s[8:9], s[8:9], 22
	s_sext_i32_i16 s10, s10
	s_sext_i32_i8 s7, s7
	s_add_u32 s8, s72, s8
	v_lshl_or_b32 v66, s7, 8, v99
	s_addc_u32 s9, s73, s9
	s_lshl_b32 s7, s10, 4
	s_andn2_b32 s7, s7, 63
	v_or_b32_e32 v68, s7, v110
	v_ashrrev_i32_e32 v69, 31, v68
	v_lshlrev_b64 v[68:69], 12, v[68:69]
	v_lshl_add_u64 v[68:69], s[8:9], 0, v[68:69]
	v_ashrrev_i32_e32 v67, 31, v66
	v_lshl_add_u64 v[90:91], v[66:67], 2, v[68:69]
	v_add_co_u32_e32 v66, vcc, s0, v90
	s_nop 1
	v_addc_co_u32_e32 v67, vcc, 0, v91, vcc
	v_add_co_u32_e32 v74, vcc, s1, v90
	global_load_dwordx4 v[70:73], v[66:67], off offset:-4096 nt
	s_nop 0
	global_load_dwordx4 v[66:69], v[66:67], off nt
	v_addc_co_u32_e32 v75, vcc, 0, v91, vcc
	v_add_co_u32_e32 v82, vcc, 0x4000, v90
	global_load_dwordx4 v[78:81], v[90:91], off nt
	s_nop 0
	global_load_dwordx4 v[74:77], v[74:75], off nt
	v_addc_co_u32_e32 v83, vcc, 0, v91, vcc
	v_add_co_u32_e32 v86, vcc, 0x5000, v90
	s_nop 1
	v_addc_co_u32_e32 v87, vcc, 0, v91, vcc
	v_add_co_u32_e32 v92, vcc, 0x6000, v90
	global_load_dwordx4 v[82:85], v[82:83], off nt
	s_nop 0
	global_load_dwordx4 v[86:89], v[86:87], off nt
	v_addc_co_u32_e32 v93, vcc, 0, v91, vcc
	v_add_co_u32_e32 v94, vcc, 0x7000, v90
	s_nop 1
	v_addc_co_u32_e32 v95, vcc, 0, v91, vcc
	global_load_dwordx4 v[90:93], v[92:93], off nt
	s_nop 0
	global_load_dwordx4 v[94:97], v[94:95], off nt
	s_branch .LBB0_75

; #define SEAM(k) do { if (IN(k) && IN((k) + 1)) xcd_barrier(bar); \
;         if (PROBE_MASK) { const unsigned long long t_ = __builtin_amdgcn_s_memrealtime(); if ((PROBE_MASK >> (k)) & 1u) pr_acc += t_ - pr_t0; pr_t0 = t_; } } while (0)
; __device__ __forceinline__ void convert_deferred(const Ptrs& P, unsigned char* lds, int quota) {
;     const int tid = threadIdx.x, wid = tid >> 6, lane = tid & 63;
;     float* tile = (float*)lds;
;     volatile __attribute__((address_space(3))) int* slot = (volatile __attribute__((address_space(3))) int*)((__attribute__((address_space(3))) unsigned char*)lds + 131072 + 320 + 11000);
;     unsigned* q = (unsigned*)(P.ws + WS_CTL) + CW_DEFQ;
;     for (int n = 0; n < quota; ++n) {
;         __syncthreads();
;         if (tid == 0) *slot = (int)atomicAdd(q, 1u);
;         __syncthreads();
;         const int t = *slot;
; __global__ void __launch_bounds__(NT, 2) mega(Args args) {
;     ...
;         if (IDLE_LAST(68 * 7)) convert_deferred(P, lds, 4); } SEAM(2);
.LBB0_779:
	s_abs_i32 s3, s62
	v_cvt_f32_u32_e32 v2, s3
	s_sub_i32 s4, 0, s3
	s_mov_b32 s5, 0
	v_rcp_iflag_f32_e32 v2, v2
	s_nop 0
	v_mul_f32_e32 v2, 0x4f7ffffe, v2
	v_cvt_u32_f32_e32 v2, v2
	s_nop 0
	v_readfirstlane_b32 s6, v2
	s_mul_i32 s4, s4, s6
	s_mul_hi_u32 s4, s6, s4
	s_add_i32 s6, s6, s4
	s_mul_hi_u32 s4, s6, 0x1dc
	s_mul_i32 s4, s4, s3
	s_sub_i32 s4, 0x1dc, s4
	s_sub_i32 s6, s4, s3
	s_cmp_ge_u32 s4, s3
	s_cselect_b32 s4, s6, s4
	s_sub_i32 s6, s4, s3
	s_cmp_ge_u32 s4, s3
	s_cselect_b32 s3, s6, s4
	s_cmp_eq_u32 s3, 0
	s_cselect_b64 s[6:7], -1, 0
	s_cmp_lt_i32 s2, s3
	s_cselect_b64 s[8:9], -1, 0
	s_or_b64 s[6:7], s[6:7], s[8:9]
	s_and_b64 vcc, exec, s[6:7]
	s_cbranch_vccnz .LBB0_789
	v_and_b32_e32 v2, 0x7c, v155
	v_lshlrev_b32_e32 v3, 5, v0
	s_movk_i32 s3, 0x400
	v_lshrrev_b32_e32 v4, 6, v0
	v_and_or_b32 v12, v3, s3, v2
	v_bfe_u32 v2, v0, 3, 3
	v_lshl_or_b32 v5, v4, 5, v2
	v_lshlrev_b32_e32 v2, 3, v0
	v_lshl_add_u32 v11, v182, 4, 0
	v_and_b32_e32 v2, 56, v2
	v_mul_u32_u24_e32 v16, 0x2020, v4
	v_mov_b32_e32 v3, 0
	v_lshl_add_u32 v27, v5, 2, 0
	v_mul_u32_u24_e32 v28, 0x404, v2
	v_lshlrev_b32_e32 v10, 6, v5
	s_add_i32 s12, 0, 0x22c38
	v_add_u32_e32 v16, v11, v16
	v_and_b32_e32 v13, 0xfc, v155
	v_and_b32_e32 v14, 56, v154
	s_mov_b32 s3, 5
	v_or_b32_e32 v4, 0x200, v10
	v_mov_b32_e32 v5, v3
	v_or_b32_e32 v6, 0x400, v10
	v_mov_b32_e32 v7, v3
	v_or_b32_e32 v8, 0x600, v10
	v_mov_b32_e32 v9, v3
	v_mov_b32_e32 v15, s12
	s_movk_i32 s13, 0xb21
	s_movk_i32 s14, 0x800
	s_mov_b32 s15, 0x1104e000
	s_movk_i32 s16, 0x4de
	v_add_u32_e32 v17, 0x404, v16
	v_add_u32_e32 v18, 0x40c, v16
	v_add_u32_e32 v19, 0x808, v16
	v_add_u32_e32 v20, 0xc0c, v16
	v_add_u32_e32 v21, 0xc14, v16
	v_add_u32_e32 v22, 0x1414, v16
	v_add_u32_e32 v23, 0x141c, v16
	v_add_u32_e32 v24, 0x1818, v16
	v_add_u32_e32 v25, 0x1c1c, v16
	v_add_u32_e32 v26, 0x1c24, v16
	v_lshlrev_b32_e32 v2, 1, v2
	v_add_u32_e32 v27, v27, v28
	v_lshlrev_b32_e32 v10, 1, v10
	s_branch .LBB0_782

; __device__ __forceinline__ unsigned g8_cvt_pk(float lo, float hi) { unsigned r; asm volatile("v_cvt_pk_bf16_f32 %0, %1, %2" : "=v"(r) : "v"(lo), "v"(hi)); return r; }
; __device__ __forceinline__ void convert_deferred(const Ptrs& P, unsigned char* lds, int quota) {
;     ...
;         __syncthreads();
;         if (tid == 0) *slot = (int)atomicAdd(q, 1u);
;         __syncthreads();
;         const int t = *slot;
;         if (t >= DEF_GU + DEF_DN) break;
;         const bool gu = t < DEF_GU;
;         const float* src = gu ? P.in[34] : P.in[36]; bf16* dst = (bf16*)(P.ws + (gu ? WS_WGU : WS_WDN));
;         const int N = gu ? 2048 : 1024, ntn = N / 256, it = gu ? 2 * NE * 16 * 8 - DEF_GU + t : 2 * NE * 16 * 4 - DEF_DN + (t - DEF_GU);
;         f32x4 cur[8];
;         bt_load(src, N, gu ? 1 : 0, it, ntn, cur);
; #pragma unroll
;         for (int i = 0; i < 8; ++i) { float* tp = tile + (wid * 8 + i) * 257 + lane * 4; tp[0] = cur[i][0]; tp[1] = cur[i][1]; tp[2] = cur[i][2]; tp[3] = cur[i][3]; }
;         __syncthreads();
;         const int per = 16 * ntn, z = it / per, r = it % per, kt = r / ntn, nt = r % ntn;
;         bf16* d = dst + (size_t)z * N * 1024 + (((size_t)nt * 16 + kt) << 14);
;         const int kc = lane & 7;
; #pragma unroll
;         for (int pss = 0; pss < 4; ++pss) {
;             const int nn = wid * 32 + pss * 8 + (lane >> 3); float f[8];
; #pragma unroll
;             for (int j = 0; j < 8; ++j) f[j] = tile[(kc * 8 + j) * 257 + nn];
;             u32x4 w; w.x = g8_cvt_pk(f[0], f[1]); w.y = g8_cvt_pk(f[2], f[3]); w.z = g8_cvt_pk(f[4], f[5]); w.w = g8_cvt_pk(f[6], f[7]);
;             *(u32x4*)(d + nn * 64 + kc * 8) = w;
;         }
.LBB0_786:
	s_or_b64 exec, exec, s[6:7]
	s_waitcnt lgkmcnt(0)
	s_barrier
	ds_read_b32 v11, v15
	s_mov_b64 s[6:7], -1
	s_waitcnt lgkmcnt(0)
	v_cmp_lt_i32_e32 vcc, s13, v11
	v_readfirstlane_b32 s4, v11
	s_cbranch_vccnz .LBB0_781
	s_cmpk_gt_i32 s4, 0x76b
	s_cselect_b64 vcc, -1, 0
	s_and_b64 s[6:7], vcc, exec
	s_cselect_b32 s6, s15, 0x104e000
	s_cselect_b32 s11, 0x400, s14
	s_cselect_b32 s17, s73, s69
	s_cselect_b32 s20, s72, s68
	s_cselect_b32 s7, s16, 0x1894
	s_cselect_b32 s18, 20, 21
	s_cselect_b32 s21, 10, 11
	s_add_u32 s26, s78, s6
	s_addc_u32 s27, s79, 0
	s_lshr_b32 s8, s11, 4
	s_abs_i32 s6, s8
	v_cvt_f32_u32_e32 v11, s6
	s_sub_i32 s19, 0, s6
	s_add_i32 s7, s7, s4
	s_abs_i32 s9, s7
	v_rcp_iflag_f32_e32 v11, v11
	s_xor_b32 s4, s7, s8
	s_lshr_b32 s10, s11, 8
	s_ashr_i32 s4, s4, 31
	v_mul_f32_e32 v11, 0x4f7ffffe, v11
	v_cvt_u32_f32_e32 v11, v11
	s_nop 0
	v_readfirstlane_b32 s28, v11
	s_mul_i32 s19, s19, s28
	s_mul_hi_u32 s19, s28, s19
	s_add_i32 s28, s28, s19
	s_mul_hi_u32 s19, s9, s28
	s_mul_i32 s28, s19, s6
	s_sub_i32 s9, s9, s28
	s_add_i32 s28, s19, 1
	s_sub_i32 s29, s9, s6
	s_cmp_ge_u32 s9, s6
	s_cselect_b32 s19, s28, s19
	s_cselect_b32 s9, s29, s9
	s_add_i32 s28, s19, 1
	s_cmp_ge_u32 s9, s6
	s_cselect_b32 s6, s28, s19
	s_xor_b32 s6, s6, s4
	s_sub_i32 s6, s6, s4
	s_sext_i32_i8 s4, s10
	v_cvt_f32_i32_e32 v11, s4
	s_mul_i32 s8, s6, s8
	s_sub_i32 s7, s7, s8
	v_cvt_f32_i32_e32 v28, s7
	v_rcp_iflag_f32_e32 v29, v11
	s_xor_b32 s4, s7, s4
	s_ashr_i32 s4, s4, 30
	s_or_b32 s4, s4, 1
	v_mul_f32_e32 v29, v28, v29
	v_trunc_f32_e32 v29, v29
	v_fma_f32 v28, -v29, v11, v28
	v_cvt_i32_f32_e32 v29, v29
	v_cmp_ge_f32_e64 s[8:9], |v28|, |v11|
	s_and_b64 s[8:9], s[8:9], exec
	s_cselect_b32 s4, s4, 0
	v_readfirstlane_b32 s8, v29
	s_add_i32 s8, s8, s4
	s_mul_i32 s9, s8, s10
	s_sub_i32 s10, s7, s9
	s_sext_i32_i8 s7, s10
	v_lshl_add_u32 v11, s7, 7, v12
	v_lshl_or_b32 v28, s7, 8, v13
	s_ashr_i32 s7, s6, 31
	s_sext_i32_i8 s4, s8
	s_lshl_b64 s[18:19], s[6:7], s18
	v_lshl_or_b32 v30, s4, 6, v14
	s_lshl_b64 s[18:19], s[18:19], 2
	v_ashrrev_i32_e32 v31, 31, v30
	s_add_u32 s18, s20, s18
	v_cndmask_b32_e32 v28, v11, v28, vcc
	s_addc_u32 s19, s17, s19
	v_lshlrev_b64 v[30:31], s21, v[30:31]
	v_lshl_add_u64 v[30:31], v[30:31], 2, s[18:19]
	v_ashrrev_i32_e32 v29, 31, v28
	v_lshl_add_u64 v[52:53], v[28:29], 2, v[30:31]
	s_lshl_b64 s[18:19], 12, s21
	s_lshl_b32 s4, s11, 2
	v_lshl_add_u64 v[40:41], v[52:53], 0, s[18:19]
	s_lshl_b64 s[18:19], 24, s21
	v_lshl_add_u64 v[36:37], v[52:53], 0, s[4:5]
	v_lshl_add_u64 v[44:45], v[52:53], 0, s[18:19]
	s_lshl_b64 s[18:19], 28, s21
	v_lshl_add_u64 v[54:55], v[36:37], 0, s[4:5]
	v_lshl_add_u64 v[48:49], v[52:53], 0, s[18:19]
	s_lshl_b32 s4, s11, 3
	s_lshl_b64 s[18:19], 20, s21
	global_load_dwordx4 v[28:31], v[52:53], off nt
	global_load_dwordx4 v[32:35], v[36:37], off nt
	s_nop 0
	global_load_dwordx4 v[36:39], v[54:55], off nt
	s_nop 0
	global_load_dwordx4 v[40:43], v[40:41], off nt
	v_lshl_add_u64 v[54:55], v[54:55], 0, s[4:5]
	v_lshl_add_u64 v[56:57], v[52:53], 0, s[18:19]
	global_load_dwordx4 v[44:47], v[44:45], off nt
	s_nop 0
	global_load_dwordx4 v[48:51], v[48:49], off nt
	s_nop 0
	global_load_dwordx4 v[52:55], v[54:55], off nt
	s_nop 0
	global_load_dwordx4 v[56:59], v[56:57], off nt
	s_lshl_b64 s[6:7], s[6:7], s21
	s_lshl_b64 s[6:7], s[6:7], 11
	s_add_u32 s4, s26, s6
	s_addc_u32 s11, s27, s7
	s_bfe_i64 s[6:7], s[10:11], 0x80000
	s_bfe_i64 s[8:9], s[8:9], 0x80000
	s_lshl_b64 s[6:7], s[6:7], 19
	s_add_u32 s4, s4, s6
	s_addc_u32 s10, s11, s7
	s_lshl_b64 s[6:7], s[8:9], 15
	s_add_u32 s6, s4, s6
	s_addc_u32 s7, s10, s7
	v_mov_b32_e32 v11, v3
	s_add_i32 s3, s3, -1
	s_cmp_eq_u32 s3, 0
	s_waitcnt vmcnt(7)
	ds_write_b128 v16, v[28:31]
	s_waitcnt vmcnt(6)
	ds_write2_b32 v17, v32, v33 offset1:1
	ds_write2_b32 v18, v34, v35 offset1:1
	s_waitcnt vmcnt(3)
	ds_write2_b64 v24, v[44:45], v[46:47] offset1:1
	s_waitcnt vmcnt(2)
	ds_write2_b32 v25, v48, v49 offset1:1
	ds_write2_b32 v26, v50, v51 offset1:1
	ds_write2_b64 v19, v[36:37], v[38:39] offset1:1
	ds_write2_b32 v20, v40, v41 offset1:1
	ds_write2_b32 v21, v42, v43 offset1:1
	s_waitcnt vmcnt(1)
	ds_write_b128 v16, v[52:55] offset:4112
	s_waitcnt vmcnt(0)
	ds_write2_b32 v22, v56, v57 offset1:1
	ds_write2_b32 v23, v58, v59 offset1:1
	s_waitcnt lgkmcnt(0)
	s_barrier
	ds_read_b32 v28, v27 offset:1028
	ds_read_b32 v29, v27 offset:3084
	ds_read_b32 v30, v27 offset:5140
	ds_read_b32 v31, v27 offset:7196
	ds_read_b32 v32, v27 offset:6168
	ds_read_b32 v33, v27 offset:4112
	ds_read_b32 v34, v27 offset:2056
	ds_read_b32 v35, v27
	s_waitcnt lgkmcnt(0)
	v_cvt_pk_bf16_f32 v28, v35, v28
	v_cvt_pk_bf16_f32 v29, v34, v29
	v_cvt_pk_bf16_f32 v30, v33, v30
	v_cvt_pk_bf16_f32 v31, v32, v31
	ds_read_b32 v36, v27 offset:1060
	ds_read_b32 v37, v27 offset:3116
	ds_read_b32 v38, v27 offset:5172
	ds_read_b32 v39, v27 offset:7228
	ds_read_b32 v40, v27 offset:6200
	ds_read_b32 v41, v27 offset:4144
	ds_read_b32 v42, v27 offset:2088
	ds_read_b32 v43, v27 offset:32
	v_lshl_add_u64 v[32:33], s[6:7], 0, v[2:3]
	v_lshl_add_u64 v[34:35], v[32:33], 0, v[10:11]
	global_store_dwordx4 v[34:35], v[28:31], off
	v_lshl_add_u64 v[34:35], v[4:5], 1, v[32:33]
	s_cselect_b64 s[6:7], -1, 0
	s_waitcnt lgkmcnt(0)
	v_cvt_pk_bf16_f32 v28, v43, v36
	v_cvt_pk_bf16_f32 v29, v42, v37
	v_cvt_pk_bf16_f32 v30, v41, v38
	v_cvt_pk_bf16_f32 v31, v40, v39
	ds_read_b32 v11, v27 offset:1092
	ds_read_b32 v36, v27 offset:3148
	ds_read_b32 v37, v27 offset:6232
	ds_read_b32 v38, v27 offset:4176
	ds_read_b32 v39, v27 offset:2120
	ds_read_b32 v40, v27 offset:64
	ds_read_b32 v41, v27 offset:5204
	ds_read_b32 v42, v27 offset:7260
	global_store_dwordx4 v[34:35], v[28:31], off
	v_lshl_add_u64 v[34:35], v[6:7], 1, v[32:33]
	v_lshl_add_u64 v[32:33], v[8:9], 1, v[32:33]
	s_waitcnt lgkmcnt(2)
	v_cvt_pk_bf16_f32 v28, v40, v11
	v_cvt_pk_bf16_f32 v29, v39, v36
	s_waitcnt lgkmcnt(1)
	v_cvt_pk_bf16_f32 v30, v38, v41
	s_waitcnt lgkmcnt(0)
	v_cvt_pk_bf16_f32 v31, v37, v42
	ds_read_b32 v11, v27 offset:1124
	ds_read_b32 v36, v27 offset:3180
	ds_read_b32 v37, v27 offset:6264
	ds_read_b32 v38, v27 offset:4208
	ds_read_b32 v39, v27 offset:2152
	ds_read_b32 v40, v27 offset:96
	ds_read_b32 v41, v27 offset:5236
	ds_read_b32 v42, v27 offset:7292
	global_store_dwordx4 v[34:35], v[28:31], off
	s_waitcnt lgkmcnt(2)
	s_nop 0
	v_cvt_pk_bf16_f32 v28, v40, v11
	v_cvt_pk_bf16_f32 v29, v39, v36
	s_waitcnt lgkmcnt(1)
	v_cvt_pk_bf16_f32 v30, v38, v41
	s_waitcnt lgkmcnt(0)
	v_cvt_pk_bf16_f32 v31, v37, v42
	global_store_dwordx4 v[32:33], v[28:31], off
	s_branch .LBB0_781

; #define SEAM(k) do { if (IN(k) && IN((k) + 1)) xcd_barrier(bar); \
;         if (PROBE_MASK) { const unsigned long long t_ = __builtin_amdgcn_s_memrealtime(); if ((PROBE_MASK >> (k)) & 1u) pr_acc += t_ - pr_t0; pr_t0 = t_; } } while (0)
; __device__ __forceinline__ void convert_deferred(const Ptrs& P, unsigned char* lds, int quota) {
;     const int tid = threadIdx.x, wid = tid >> 6, lane = tid & 63;
;     float* tile = (float*)lds;
;     volatile __attribute__((address_space(3))) int* slot = (volatile __attribute__((address_space(3))) int*)((__attribute__((address_space(3))) unsigned char*)lds + 131072 + 320 + 11000);
;     unsigned* q = (unsigned*)(P.ws + WS_CTL) + CW_DEFQ;
;     for (int n = 0; n < quota; ++n) {
;         __syncthreads();
;         if (tid == 0) *slot = (int)atomicAdd(q, 1u);
;         __syncthreads();
;         const int t = *slot;
; __global__ void __launch_bounds__(NT, 2) mega(Args args) {
;     ...
;         if (IDLE_LAST(68 * 4)) convert_deferred(P, lds, 4); } SEAM(6);
.LBB0_1286:
	s_abs_i32 s3, s62
	v_cvt_f32_u32_e32 v2, s3
	s_sub_i32 s4, 0, s3
	s_mov_b32 s5, 0
	v_rcp_iflag_f32_e32 v2, v2
	s_nop 0
	v_mul_f32_e32 v2, 0x4f7ffffe, v2
	v_cvt_u32_f32_e32 v2, v2
	s_nop 0
	v_readfirstlane_b32 s6, v2
	s_mul_i32 s4, s4, s6
	s_mul_hi_u32 s4, s6, s4
	s_add_i32 s6, s6, s4
	s_mul_hi_u32 s4, s6, 0x110
	s_mul_i32 s4, s4, s3
	s_sub_i32 s4, 0x110, s4
	s_sub_i32 s6, s4, s3
	s_cmp_ge_u32 s4, s3
	s_cselect_b32 s4, s6, s4
	s_sub_i32 s6, s4, s3
	s_cmp_ge_u32 s4, s3
	s_cselect_b32 s3, s6, s4
	s_cmp_eq_u32 s3, 0
	s_cselect_b64 s[6:7], -1, 0
	s_cmp_lt_i32 s2, s3
	s_cselect_b64 s[8:9], -1, 0
	s_or_b64 s[6:7], s[6:7], s[8:9]
	s_and_b64 vcc, exec, s[6:7]
	s_cbranch_vccnz .LBB0_1296
	v_and_b32_e32 v2, 0x7c, v188
	v_lshlrev_b32_e32 v3, 5, v0
	s_movk_i32 s3, 0x400
	v_and_or_b32 v12, v3, s3, v2
	v_bfe_u32 v2, v0, 3, 3
	v_lshl_or_b32 v4, v1, 5, v2
	v_lshlrev_b32_e32 v2, 3, v0
	v_lshl_add_u32 v11, v182, 4, 0
	v_and_b32_e32 v2, 56, v2
	v_mul_u32_u24_e32 v16, 0x2020, v1
	v_mov_b32_e32 v3, 0
	v_lshl_add_u32 v27, v4, 2, 0
	v_mul_u32_u24_e32 v28, 0x404, v2
	v_lshlrev_b32_e32 v10, 6, v4
	s_add_i32 s12, 0, 0x22c38
	v_add_u32_e32 v16, v11, v16
	v_and_b32_e32 v13, 0xfc, v188
	v_and_b32_e32 v14, 56, v185
	s_mov_b32 s3, 6
	v_or_b32_e32 v4, 0x200, v10
	v_mov_b32_e32 v5, v3
	v_or_b32_e32 v6, 0x400, v10
	v_mov_b32_e32 v7, v3
	v_or_b32_e32 v8, 0x600, v10
	v_mov_b32_e32 v9, v3
	v_mov_b32_e32 v15, s12
	s_movk_i32 s13, 0xb21
	s_movk_i32 s14, 0x800
	s_mov_b32 s15, 0x1104e000
	s_movk_i32 s16, 0x4de
	v_add_u32_e32 v17, 0x404, v16
	v_add_u32_e32 v18, 0x40c, v16
	v_add_u32_e32 v19, 0x808, v16
	v_add_u32_e32 v20, 0xc0c, v16
	v_add_u32_e32 v21, 0xc14, v16
	v_add_u32_e32 v22, 0x1414, v16
	v_add_u32_e32 v23, 0x141c, v16
	v_add_u32_e32 v24, 0x1818, v16
	v_add_u32_e32 v25, 0x1c1c, v16
	v_add_u32_e32 v26, 0x1c24, v16
	v_lshlrev_b32_e32 v2, 1, v2
	v_add_u32_e32 v27, v27, v28
	v_lshlrev_b32_e32 v10, 1, v10
	s_branch .LBB0_1289

; __device__ __forceinline__ unsigned g8_cvt_pk(float lo, float hi) { unsigned r; asm volatile("v_cvt_pk_bf16_f32 %0, %1, %2" : "=v"(r) : "v"(lo), "v"(hi)); return r; }
; __device__ __forceinline__ void convert_deferred(const Ptrs& P, unsigned char* lds, int quota) {
;     ...
;         __syncthreads();
;         if (tid == 0) *slot = (int)atomicAdd(q, 1u);
;         __syncthreads();
;         const int t = *slot;
;         if (t >= DEF_GU + DEF_DN) break;
;         const bool gu = t < DEF_GU;
;         const float* src = gu ? P.in[34] : P.in[36]; bf16* dst = (bf16*)(P.ws + (gu ? WS_WGU : WS_WDN));
;         const int N = gu ? 2048 : 1024, ntn = N / 256, it = gu ? 2 * NE * 16 * 8 - DEF_GU + t : 2 * NE * 16 * 4 - DEF_DN + (t - DEF_GU);
;         f32x4 cur[8];
;         bt_load(src, N, gu ? 1 : 0, it, ntn, cur);
; #pragma unroll
;         for (int i = 0; i < 8; ++i) { float* tp = tile + (wid * 8 + i) * 257 + lane * 4; tp[0] = cur[i][0]; tp[1] = cur[i][1]; tp[2] = cur[i][2]; tp[3] = cur[i][3]; }
;         __syncthreads();
;         const int per = 16 * ntn, z = it / per, r = it % per, kt = r / ntn, nt = r % ntn;
;         bf16* d = dst + (size_t)z * N * 1024 + (((size_t)nt * 16 + kt) << 14);
;         const int kc = lane & 7;
; #pragma unroll
;         for (int pss = 0; pss < 4; ++pss) {
;             const int nn = wid * 32 + pss * 8 + (lane >> 3); float f[8];
; #pragma unroll
;             for (int j = 0; j < 8; ++j) f[j] = tile[(kc * 8 + j) * 257 + nn];
;             u32x4 w; w.x = g8_cvt_pk(f[0], f[1]); w.y = g8_cvt_pk(f[2], f[3]); w.z = g8_cvt_pk(f[4], f[5]); w.w = g8_cvt_pk(f[6], f[7]);
;             *(u32x4*)(d + nn * 64 + kc * 8) = w;
;         }
.LBB0_1293:
	s_or_b64 exec, exec, s[6:7]
	s_waitcnt lgkmcnt(0)
	s_barrier
	ds_read_b32 v11, v15
	s_mov_b64 s[6:7], -1
	s_waitcnt lgkmcnt(0)
	v_cmp_lt_i32_e32 vcc, s13, v11
	v_readfirstlane_b32 s4, v11
	s_cbranch_vccnz .LBB0_1288
	s_cmpk_gt_i32 s4, 0x76b
	s_cselect_b64 vcc, -1, 0
	s_and_b64 s[6:7], vcc, exec
	s_cselect_b32 s6, s15, 0x104e000
	s_cselect_b32 s11, 0x400, s14
	s_cselect_b32 s17, s73, s69
	s_cselect_b32 s20, s72, s68
	s_cselect_b32 s7, s16, 0x1894
	s_cselect_b32 s18, 20, 21
	s_cselect_b32 s21, 10, 11
	s_add_u32 s22, s78, s6
	s_addc_u32 s23, s79, 0
	s_lshr_b32 s8, s11, 4
	s_abs_i32 s6, s8
	v_cvt_f32_u32_e32 v11, s6
	s_sub_i32 s19, 0, s6
	s_add_i32 s7, s7, s4
	s_abs_i32 s9, s7
	v_rcp_iflag_f32_e32 v11, v11
	s_xor_b32 s4, s7, s8
	s_lshr_b32 s10, s11, 8
	s_ashr_i32 s4, s4, 31
	v_mul_f32_e32 v11, 0x4f7ffffe, v11
	v_cvt_u32_f32_e32 v11, v11
	s_nop 0
	v_readfirstlane_b32 s24, v11
	s_mul_i32 s19, s19, s24
	s_mul_hi_u32 s19, s24, s19
	s_add_i32 s24, s24, s19
	s_mul_hi_u32 s19, s9, s24
	s_mul_i32 s24, s19, s6
	s_sub_i32 s9, s9, s24
	s_add_i32 s24, s19, 1
	s_sub_i32 s25, s9, s6
	s_cmp_ge_u32 s9, s6
	s_cselect_b32 s19, s24, s19
	s_cselect_b32 s9, s25, s9
	s_add_i32 s24, s19, 1
	s_cmp_ge_u32 s9, s6
	s_cselect_b32 s6, s24, s19
	s_xor_b32 s6, s6, s4
	s_sub_i32 s6, s6, s4
	s_sext_i32_i8 s4, s10
	v_cvt_f32_i32_e32 v11, s4
	s_mul_i32 s8, s6, s8
	s_sub_i32 s7, s7, s8
	v_cvt_f32_i32_e32 v28, s7
	v_rcp_iflag_f32_e32 v29, v11
	s_xor_b32 s4, s7, s4
	s_ashr_i32 s4, s4, 30
	s_or_b32 s4, s4, 1
	v_mul_f32_e32 v29, v28, v29
	v_trunc_f32_e32 v29, v29
	v_fma_f32 v28, -v29, v11, v28
	v_cvt_i32_f32_e32 v29, v29
	v_cmp_ge_f32_e64 s[8:9], |v28|, |v11|
	s_and_b64 s[8:9], s[8:9], exec
	s_cselect_b32 s4, s4, 0
	v_readfirstlane_b32 s8, v29
	s_add_i32 s8, s8, s4
	s_mul_i32 s9, s8, s10
	s_sub_i32 s10, s7, s9
	s_sext_i32_i8 s7, s10
	v_lshl_add_u32 v11, s7, 7, v12
	v_lshl_or_b32 v28, s7, 8, v13
	s_ashr_i32 s7, s6, 31
	s_sext_i32_i8 s4, s8
	s_lshl_b64 s[18:19], s[6:7], s18
	v_lshl_or_b32 v30, s4, 6, v14
	s_lshl_b64 s[18:19], s[18:19], 2
	v_ashrrev_i32_e32 v31, 31, v30
	s_add_u32 s18, s20, s18
	v_cndmask_b32_e32 v28, v11, v28, vcc
	s_addc_u32 s19, s17, s19
	v_lshlrev_b64 v[30:31], s21, v[30:31]
	v_lshl_add_u64 v[30:31], v[30:31], 2, s[18:19]
	v_ashrrev_i32_e32 v29, 31, v28
	v_lshl_add_u64 v[52:53], v[28:29], 2, v[30:31]
	s_lshl_b64 s[18:19], 12, s21
	s_lshl_b32 s4, s11, 2
	v_lshl_add_u64 v[40:41], v[52:53], 0, s[18:19]
	s_lshl_b64 s[18:19], 24, s21
	v_lshl_add_u64 v[36:37], v[52:53], 0, s[4:5]
	v_lshl_add_u64 v[44:45], v[52:53], 0, s[18:19]
	s_lshl_b64 s[18:19], 28, s21
	v_lshl_add_u64 v[54:55], v[36:37], 0, s[4:5]
	v_lshl_add_u64 v[48:49], v[52:53], 0, s[18:19]
	s_lshl_b32 s4, s11, 3
	s_lshl_b64 s[18:19], 20, s21
	global_load_dwordx4 v[28:31], v[52:53], off nt
	global_load_dwordx4 v[32:35], v[36:37], off nt
	s_nop 0
	global_load_dwordx4 v[36:39], v[54:55], off nt
	s_nop 0
	global_load_dwordx4 v[40:43], v[40:41], off nt
	v_lshl_add_u64 v[54:55], v[54:55], 0, s[4:5]
	v_lshl_add_u64 v[56:57], v[52:53], 0, s[18:19]
	global_load_dwordx4 v[44:47], v[44:45], off nt
	s_nop 0
	global_load_dwordx4 v[48:51], v[48:49], off nt
	s_nop 0
	global_load_dwordx4 v[52:55], v[54:55], off nt
	s_nop 0
	global_load_dwordx4 v[56:59], v[56:57], off nt
	s_lshl_b64 s[6:7], s[6:7], s21
	s_lshl_b64 s[6:7], s[6:7], 11
	s_add_u32 s4, s22, s6
	s_addc_u32 s11, s23, s7
	s_bfe_i64 s[6:7], s[10:11], 0x80000
	s_bfe_i64 s[8:9], s[8:9], 0x80000
	s_lshl_b64 s[6:7], s[6:7], 19
	s_add_u32 s4, s4, s6
	s_addc_u32 s10, s11, s7
	s_lshl_b64 s[6:7], s[8:9], 15
	s_add_u32 s6, s4, s6
	s_addc_u32 s7, s10, s7
	v_mov_b32_e32 v11, v3
	s_add_i32 s3, s3, -1
	s_cmp_eq_u32 s3, 0
	s_waitcnt vmcnt(7)
	ds_write_b128 v16, v[28:31]
	s_waitcnt vmcnt(6)
	ds_write2_b32 v17, v32, v33 offset1:1
	ds_write2_b32 v18, v34, v35 offset1:1
	s_waitcnt vmcnt(3)
	ds_write2_b64 v24, v[44:45], v[46:47] offset1:1
	s_waitcnt vmcnt(2)
	ds_write2_b32 v25, v48, v49 offset1:1
	ds_write2_b32 v26, v50, v51 offset1:1
	ds_write2_b64 v19, v[36:37], v[38:39] offset1:1
	ds_write2_b32 v20, v40, v41 offset1:1
	ds_write2_b32 v21, v42, v43 offset1:1
	s_waitcnt vmcnt(1)
	ds_write_b128 v16, v[52:55] offset:4112
	s_waitcnt vmcnt(0)
	ds_write2_b32 v22, v56, v57 offset1:1
	ds_write2_b32 v23, v58, v59 offset1:1
	s_waitcnt lgkmcnt(0)
	s_barrier
	ds_read_b32 v28, v27 offset:1028
	ds_read_b32 v29, v27 offset:3084
	ds_read_b32 v30, v27 offset:5140
	ds_read_b32 v31, v27 offset:7196
	ds_read_b32 v32, v27 offset:6168
	ds_read_b32 v33, v27 offset:4112
	ds_read_b32 v34, v27 offset:2056
	ds_read_b32 v35, v27
	s_waitcnt lgkmcnt(0)
	v_cvt_pk_bf16_f32 v28, v35, v28
	v_cvt_pk_bf16_f32 v29, v34, v29
	v_cvt_pk_bf16_f32 v30, v33, v30
	v_cvt_pk_bf16_f32 v31, v32, v31
	ds_read_b32 v36, v27 offset:1060
	ds_read_b32 v37, v27 offset:3116
	ds_read_b32 v38, v27 offset:5172
	ds_read_b32 v39, v27 offset:7228
	ds_read_b32 v40, v27 offset:6200
	ds_read_b32 v41, v27 offset:4144
	ds_read_b32 v42, v27 offset:2088
	ds_read_b32 v43, v27 offset:32
	v_lshl_add_u64 v[32:33], s[6:7], 0, v[2:3]
	v_lshl_add_u64 v[34:35], v[32:33], 0, v[10:11]
	global_store_dwordx4 v[34:35], v[28:31], off
	v_lshl_add_u64 v[34:35], v[4:5], 1, v[32:33]
	s_cselect_b64 s[6:7], -1, 0
	s_waitcnt lgkmcnt(0)
	v_cvt_pk_bf16_f32 v28, v43, v36
	v_cvt_pk_bf16_f32 v29, v42, v37
	v_cvt_pk_bf16_f32 v30, v41, v38
	v_cvt_pk_bf16_f32 v31, v40, v39
	ds_read_b32 v11, v27 offset:1092
	ds_read_b32 v36, v27 offset:3148
	ds_read_b32 v37, v27 offset:6232
	ds_read_b32 v38, v27 offset:4176
	ds_read_b32 v39, v27 offset:2120
	ds_read_b32 v40, v27 offset:64
	ds_read_b32 v41, v27 offset:5204
	ds_read_b32 v42, v27 offset:7260
	global_store_dwordx4 v[34:35], v[28:31], off
	v_lshl_add_u64 v[34:35], v[6:7], 1, v[32:33]
	v_lshl_add_u64 v[32:33], v[8:9], 1, v[32:33]
	s_waitcnt lgkmcnt(2)
	v_cvt_pk_bf16_f32 v28, v40, v11
	v_cvt_pk_bf16_f32 v29, v39, v36
	s_waitcnt lgkmcnt(1)
	v_cvt_pk_bf16_f32 v30, v38, v41
	s_waitcnt lgkmcnt(0)
	v_cvt_pk_bf16_f32 v31, v37, v42
	ds_read_b32 v11, v27 offset:1124
	ds_read_b32 v36, v27 offset:3180
	ds_read_b32 v37, v27 offset:6264
	ds_read_b32 v38, v27 offset:4208
	ds_read_b32 v39, v27 offset:2152
	ds_read_b32 v40, v27 offset:96
	ds_read_b32 v41, v27 offset:5236
	ds_read_b32 v42, v27 offset:7292
	global_store_dwordx4 v[34:35], v[28:31], off
	s_waitcnt lgkmcnt(2)
	s_nop 0
	v_cvt_pk_bf16_f32 v28, v40, v11
	v_cvt_pk_bf16_f32 v29, v39, v36
	s_waitcnt lgkmcnt(1)
	v_cvt_pk_bf16_f32 v30, v38, v41
	s_waitcnt lgkmcnt(0)
	v_cvt_pk_bf16_f32 v31, v37, v42
	global_store_dwordx4 v[32:33], v[28:31], off
	s_branch .LBB0_1288

; #define LAS __attribute__((address_space(3)))
; #define SEAM(k) do { if (IN(k) && IN((k) + 1)) xcd_barrier(bar); \
;         if (PROBE_MASK) { const unsigned long long t_ = __builtin_amdgcn_s_memrealtime(); if ((PROBE_MASK >> (k)) & 1u) pr_acc += t_ - pr_t0; pr_t0 = t_; } } while (0)
; __device__ __forceinline__ void convert_deferred(const Ptrs& P, unsigned char* lds, int quota) {
;     const int tid = threadIdx.x, wid = tid >> 6, lane = tid & 63;
;     float* tile = (float*)lds;
;     volatile __attribute__((address_space(3))) int* slot = (volatile __attribute__((address_space(3))) int*)((__attribute__((address_space(3))) unsigned char*)lds + 131072 + 320 + 11000);
;     unsigned* q = (unsigned*)(P.ws + WS_CTL) + CW_DEFQ;
;     for (int n = 0; n < quota; ++n) {
;         __syncthreads();
;         if (tid == 0) *slot = (int)atomicAdd(q, 1u);
;         __syncthreads();
;         const int t = *slot;
; __global__ void __launch_bounds__(NT, 2) mega(Args args) {
;     ...
;         { const int rem_ = ((LAS int*)(LDSP + MISC_OFF + 256))[96] % G; if (rem_ != 0 && vcu >= rem_) convert_deferred(P, lds, 5); } } SEAM(9);
.LBB0_1609:
	s_abs_i32 s0, s62
	v_cvt_f32_u32_e32 v2, s0
	s_sub_i32 s5, 0, s0
	s_abs_i32 s4, s9
	s_ashr_i32 s3, s9, 31
	v_rcp_iflag_f32_e32 v2, v2
	s_mov_b32 s1, 0
	v_mul_f32_e32 v2, 0x4f7ffffe, v2
	v_cvt_u32_f32_e32 v2, v2
	s_nop 0
	v_readfirstlane_b32 s6, v2
	s_mul_i32 s5, s5, s6
	s_mul_hi_u32 s5, s6, s5
	s_add_i32 s6, s6, s5
	s_mul_hi_u32 s5, s4, s6
	s_mul_i32 s5, s5, s0
	s_sub_i32 s4, s4, s5
	s_sub_i32 s5, s4, s0
	s_cmp_ge_u32 s4, s0
	s_cselect_b32 s4, s5, s4
	s_sub_i32 s5, s4, s0
	s_cmp_ge_u32 s4, s0
	s_cselect_b32 s0, s5, s4
	s_xor_b32 s0, s0, s3
	s_sub_i32 s0, s0, s3
	s_cmp_eq_u32 s0, 0
	v_readlane_b32 s3, v254, 2
	s_cselect_b64 s[4:5], -1, 0
	s_cmp_lt_i32 s3, s0
	s_cselect_b64 s[6:7], -1, 0
	s_or_b64 s[4:5], s[4:5], s[6:7]
	s_and_b64 vcc, exec, s[4:5]
	s_cbranch_vccnz .LBB0_1619
	v_and_b32_e32 v2, 0x7c, v175
	v_lshlrev_b32_e32 v3, 5, v0
	s_movk_i32 s0, 0x400
	v_and_or_b32 v12, v3, s0, v2
	v_bfe_u32 v2, v0, 3, 3
	v_lshl_or_b32 v4, v1, 5, v2
	v_lshlrev_b32_e32 v2, 3, v0
	v_lshl_add_u32 v11, v182, 4, 0
	v_and_b32_e32 v2, 56, v2
	v_mul_u32_u24_e32 v16, 0x2020, v1
	v_mov_b32_e32 v3, 0
	v_lshl_add_u32 v27, v4, 2, 0
	v_mul_u32_u24_e32 v28, 0x404, v2
	v_lshlrev_b32_e32 v10, 6, v4
	s_add_i32 s10, 0, 0x22c38
	v_add_u32_e32 v16, v11, v16
	s_mov_b32 s3, 6
	v_and_b32_e32 v13, 0xfc, v175
	v_and_b32_e32 v14, 56, v173
	v_or_b32_e32 v4, 0x200, v10
	v_mov_b32_e32 v5, v3
	v_or_b32_e32 v6, 0x400, v10
	v_mov_b32_e32 v7, v3
	v_or_b32_e32 v8, 0x600, v10
	v_mov_b32_e32 v9, v3
	v_mov_b32_e32 v15, s10
	s_movk_i32 s11, 0xb21
	s_movk_i32 s12, 0x800
	s_mov_b32 s13, 0x1104e000
	s_movk_i32 s14, 0x4de
	v_add_u32_e32 v17, 0x404, v16
	v_add_u32_e32 v18, 0x40c, v16
	v_add_u32_e32 v19, 0x808, v16
	v_add_u32_e32 v20, 0xc0c, v16
	v_add_u32_e32 v21, 0xc14, v16
	v_add_u32_e32 v22, 0x1414, v16
	v_add_u32_e32 v23, 0x141c, v16
	v_add_u32_e32 v24, 0x1818, v16
	v_add_u32_e32 v25, 0x1c1c, v16
	v_add_u32_e32 v26, 0x1c24, v16
	v_lshlrev_b32_e32 v2, 1, v2
	v_add_u32_e32 v27, v27, v28
	v_lshlrev_b32_e32 v10, 1, v10
	s_branch .LBB0_1612

; __device__ __forceinline__ unsigned g8_cvt_pk(float lo, float hi) { unsigned r; asm volatile("v_cvt_pk_bf16_f32 %0, %1, %2" : "=v"(r) : "v"(lo), "v"(hi)); return r; }
; __device__ __forceinline__ void convert_deferred(const Ptrs& P, unsigned char* lds, int quota) {
;     ...
;         __syncthreads();
;         if (tid == 0) *slot = (int)atomicAdd(q, 1u);
;         __syncthreads();
;         const int t = *slot;
;         if (t >= DEF_GU + DEF_DN) break;
;         const bool gu = t < DEF_GU;
;         const float* src = gu ? P.in[34] : P.in[36]; bf16* dst = (bf16*)(P.ws + (gu ? WS_WGU : WS_WDN));
;         const int N = gu ? 2048 : 1024, ntn = N / 256, it = gu ? 2 * NE * 16 * 8 - DEF_GU + t : 2 * NE * 16 * 4 - DEF_DN + (t - DEF_GU);
;         f32x4 cur[8];
;         bt_load(src, N, gu ? 1 : 0, it, ntn, cur);
; #pragma unroll
;         for (int i = 0; i < 8; ++i) { float* tp = tile + (wid * 8 + i) * 257 + lane * 4; tp[0] = cur[i][0]; tp[1] = cur[i][1]; tp[2] = cur[i][2]; tp[3] = cur[i][3]; }
;         __syncthreads();
;         const int per = 16 * ntn, z = it / per, r = it % per, kt = r / ntn, nt = r % ntn;
;         bf16* d = dst + (size_t)z * N * 1024 + (((size_t)nt * 16 + kt) << 14);
;         const int kc = lane & 7;
; #pragma unroll
;         for (int pss = 0; pss < 4; ++pss) {
;             const int nn = wid * 32 + pss * 8 + (lane >> 3); float f[8];
; #pragma unroll
;             for (int j = 0; j < 8; ++j) f[j] = tile[(kc * 8 + j) * 257 + nn];
;             u32x4 w; w.x = g8_cvt_pk(f[0], f[1]); w.y = g8_cvt_pk(f[2], f[3]); w.z = g8_cvt_pk(f[4], f[5]); w.w = g8_cvt_pk(f[6], f[7]);
;             *(u32x4*)(d + nn * 64 + kc * 8) = w;
;         }
.LBB0_1616:
	s_or_b64 exec, exec, s[4:5]
	s_waitcnt lgkmcnt(0)
	s_barrier
	ds_read_b32 v11, v15
	s_mov_b64 s[4:5], -1
	s_waitcnt lgkmcnt(0)
	v_cmp_lt_i32_e32 vcc, s11, v11
	v_readfirstlane_b32 s0, v11
	s_cbranch_vccnz .LBB0_1611
	s_cmpk_gt_i32 s0, 0x76b
	s_cselect_b64 vcc, -1, 0
	s_and_b64 s[4:5], vcc, exec
	s_cselect_b32 s4, s13, 0x104e000
	s_cselect_b32 s9, 0x400, s12
	s_cselect_b32 s15, s73, s69
	s_cselect_b32 s18, s72, s68
	s_cselect_b32 s5, s14, 0x1894
	s_cselect_b32 s16, 20, 21
	s_cselect_b32 s19, 10, 11
	s_add_u32 s20, s78, s4
	s_addc_u32 s21, s79, 0
	s_lshr_b32 s6, s9, 4
	s_abs_i32 s4, s6
	v_cvt_f32_u32_e32 v11, s4
	s_sub_i32 s17, 0, s4
	s_add_i32 s5, s5, s0
	s_abs_i32 s7, s5
	v_rcp_iflag_f32_e32 v11, v11
	s_xor_b32 s0, s5, s6
	s_lshr_b32 s8, s9, 8
	s_ashr_i32 s0, s0, 31
	v_mul_f32_e32 v11, 0x4f7ffffe, v11
	v_cvt_u32_f32_e32 v11, v11
	s_nop 0
	v_readfirstlane_b32 s22, v11
	s_mul_i32 s17, s17, s22
	s_mul_hi_u32 s17, s22, s17
	s_add_i32 s22, s22, s17
	s_mul_hi_u32 s17, s7, s22
	s_mul_i32 s22, s17, s4
	s_sub_i32 s7, s7, s22
	s_add_i32 s22, s17, 1
	s_sub_i32 s23, s7, s4
	s_cmp_ge_u32 s7, s4
	s_cselect_b32 s17, s22, s17
	s_cselect_b32 s7, s23, s7
	s_add_i32 s22, s17, 1
	s_cmp_ge_u32 s7, s4
	s_cselect_b32 s4, s22, s17
	s_xor_b32 s4, s4, s0
	s_sub_i32 s4, s4, s0
	s_sext_i32_i8 s0, s8
	v_cvt_f32_i32_e32 v11, s0
	s_mul_i32 s6, s4, s6
	s_sub_i32 s5, s5, s6
	v_cvt_f32_i32_e32 v28, s5
	v_rcp_iflag_f32_e32 v29, v11
	s_xor_b32 s0, s5, s0
	s_ashr_i32 s0, s0, 30
	s_or_b32 s0, s0, 1
	v_mul_f32_e32 v29, v28, v29
	v_trunc_f32_e32 v29, v29
	v_fma_f32 v28, -v29, v11, v28
	v_cvt_i32_f32_e32 v29, v29
	v_cmp_ge_f32_e64 s[6:7], |v28|, |v11|
	s_and_b64 s[6:7], s[6:7], exec
	s_cselect_b32 s0, s0, 0
	v_readfirstlane_b32 s6, v29
	s_add_i32 s6, s6, s0
	s_mul_i32 s7, s6, s8
	s_sub_i32 s8, s5, s7
	s_sext_i32_i8 s5, s8
	v_lshl_add_u32 v11, s5, 7, v12
	v_lshl_or_b32 v28, s5, 8, v13
	s_ashr_i32 s5, s4, 31
	s_sext_i32_i8 s0, s6
	s_lshl_b64 s[16:17], s[4:5], s16
	v_lshl_or_b32 v30, s0, 6, v14
	s_lshl_b64 s[16:17], s[16:17], 2
	v_ashrrev_i32_e32 v31, 31, v30
	s_add_u32 s16, s18, s16
	v_cndmask_b32_e32 v28, v11, v28, vcc
	s_addc_u32 s17, s15, s17
	v_lshlrev_b64 v[30:31], s19, v[30:31]
	v_lshl_add_u64 v[30:31], v[30:31], 2, s[16:17]
	v_ashrrev_i32_e32 v29, 31, v28
	v_lshl_add_u64 v[52:53], v[28:29], 2, v[30:31]
	s_lshl_b64 s[16:17], 12, s19
	s_lshl_b32 s0, s9, 2
	v_lshl_add_u64 v[40:41], v[52:53], 0, s[16:17]
	s_lshl_b64 s[16:17], 24, s19
	v_lshl_add_u64 v[36:37], v[52:53], 0, s[0:1]
	v_lshl_add_u64 v[44:45], v[52:53], 0, s[16:17]
	s_lshl_b64 s[16:17], 28, s19
	v_lshl_add_u64 v[54:55], v[36:37], 0, s[0:1]
	v_lshl_add_u64 v[48:49], v[52:53], 0, s[16:17]
	s_lshl_b32 s0, s9, 3
	s_lshl_b64 s[16:17], 20, s19
	global_load_dwordx4 v[28:31], v[52:53], off nt
	global_load_dwordx4 v[32:35], v[36:37], off nt
	s_nop 0
	global_load_dwordx4 v[36:39], v[54:55], off nt
	s_nop 0
	global_load_dwordx4 v[40:43], v[40:41], off nt
	v_lshl_add_u64 v[54:55], v[54:55], 0, s[0:1]
	v_lshl_add_u64 v[56:57], v[52:53], 0, s[16:17]
	global_load_dwordx4 v[44:47], v[44:45], off nt
	s_nop 0
	global_load_dwordx4 v[48:51], v[48:49], off nt
	s_nop 0
	global_load_dwordx4 v[52:55], v[54:55], off nt
	s_nop 0
	global_load_dwordx4 v[56:59], v[56:57], off nt
	s_lshl_b64 s[4:5], s[4:5], s19
	s_lshl_b64 s[4:5], s[4:5], 11
	s_add_u32 s0, s20, s4
	s_addc_u32 s9, s21, s5
	s_bfe_i64 s[4:5], s[8:9], 0x80000
	s_bfe_i64 s[6:7], s[6:7], 0x80000
	s_lshl_b64 s[4:5], s[4:5], 19
	s_add_u32 s0, s0, s4
	s_addc_u32 s8, s9, s5
	s_lshl_b64 s[4:5], s[6:7], 15
	s_add_u32 s4, s0, s4
	s_addc_u32 s5, s8, s5
	v_mov_b32_e32 v11, v3
	s_add_i32 s3, s3, -1
	s_cmp_eq_u32 s3, 0
	s_waitcnt vmcnt(7)
	ds_write_b128 v16, v[28:31]
	s_waitcnt vmcnt(6)
	ds_write2_b32 v17, v32, v33 offset1:1
	ds_write2_b32 v18, v34, v35 offset1:1
	s_waitcnt vmcnt(3)
	ds_write2_b64 v24, v[44:45], v[46:47] offset1:1
	s_waitcnt vmcnt(2)
	ds_write2_b32 v25, v48, v49 offset1:1
	ds_write2_b32 v26, v50, v51 offset1:1
	ds_write2_b64 v19, v[36:37], v[38:39] offset1:1
	ds_write2_b32 v20, v40, v41 offset1:1
	ds_write2_b32 v21, v42, v43 offset1:1
	s_waitcnt vmcnt(1)
	ds_write_b128 v16, v[52:55] offset:4112
	s_waitcnt vmcnt(0)
	ds_write2_b32 v22, v56, v57 offset1:1
	ds_write2_b32 v23, v58, v59 offset1:1
	s_waitcnt lgkmcnt(0)
	s_barrier
	ds_read_b32 v28, v27 offset:1028
	ds_read_b32 v29, v27 offset:3084
	ds_read_b32 v30, v27 offset:5140
	ds_read_b32 v31, v27 offset:7196
	ds_read_b32 v32, v27 offset:6168
	ds_read_b32 v33, v27 offset:4112
	ds_read_b32 v34, v27 offset:2056
	ds_read_b32 v35, v27
	s_waitcnt lgkmcnt(0)
	v_cvt_pk_bf16_f32 v28, v35, v28
	v_cvt_pk_bf16_f32 v29, v34, v29
	v_cvt_pk_bf16_f32 v30, v33, v30
	v_cvt_pk_bf16_f32 v31, v32, v31
	ds_read_b32 v36, v27 offset:1060
	ds_read_b32 v37, v27 offset:3116
	ds_read_b32 v38, v27 offset:5172
	ds_read_b32 v39, v27 offset:7228
	ds_read_b32 v40, v27 offset:6200
	ds_read_b32 v41, v27 offset:4144
	ds_read_b32 v42, v27 offset:2088
	ds_read_b32 v43, v27 offset:32
	v_lshl_add_u64 v[32:33], s[4:5], 0, v[2:3]
	v_lshl_add_u64 v[34:35], v[32:33], 0, v[10:11]
	global_store_dwordx4 v[34:35], v[28:31], off
	v_lshl_add_u64 v[34:35], v[4:5], 1, v[32:33]
	s_cselect_b64 s[4:5], -1, 0
	s_waitcnt lgkmcnt(0)
	v_cvt_pk_bf16_f32 v28, v43, v36
	v_cvt_pk_bf16_f32 v29, v42, v37
	v_cvt_pk_bf16_f32 v30, v41, v38
	v_cvt_pk_bf16_f32 v31, v40, v39
	ds_read_b32 v11, v27 offset:1092
	ds_read_b32 v36, v27 offset:3148
	ds_read_b32 v37, v27 offset:6232
	ds_read_b32 v38, v27 offset:4176
	ds_read_b32 v39, v27 offset:2120
	ds_read_b32 v40, v27 offset:64
	ds_read_b32 v41, v27 offset:5204
	ds_read_b32 v42, v27 offset:7260
	global_store_dwordx4 v[34:35], v[28:31], off
	v_lshl_add_u64 v[34:35], v[6:7], 1, v[32:33]
	v_lshl_add_u64 v[32:33], v[8:9], 1, v[32:33]
	s_waitcnt lgkmcnt(2)
	v_cvt_pk_bf16_f32 v28, v40, v11
	v_cvt_pk_bf16_f32 v29, v39, v36
	s_waitcnt lgkmcnt(1)
	v_cvt_pk_bf16_f32 v30, v38, v41
	s_waitcnt lgkmcnt(0)
	v_cvt_pk_bf16_f32 v31, v37, v42
	ds_read_b32 v11, v27 offset:1124
	ds_read_b32 v36, v27 offset:3180
	ds_read_b32 v37, v27 offset:6264
	ds_read_b32 v38, v27 offset:4208
	ds_read_b32 v39, v27 offset:2152
	ds_read_b32 v40, v27 offset:96
	ds_read_b32 v41, v27 offset:5236
	ds_read_b32 v42, v27 offset:7292
	global_store_dwordx4 v[34:35], v[28:31], off
	s_waitcnt lgkmcnt(2)
	s_nop 0
	v_cvt_pk_bf16_f32 v28, v40, v11
	v_cvt_pk_bf16_f32 v29, v39, v36
	s_waitcnt lgkmcnt(1)
	v_cvt_pk_bf16_f32 v30, v38, v41
	s_waitcnt lgkmcnt(0)
	v_cvt_pk_bf16_f32 v31, v37, v42
	global_store_dwordx4 v[32:33], v[28:31], off
	s_branch .LBB0_1611

; #define SEAM(k) do { if (IN(k) && IN((k) + 1)) xcd_barrier(bar); \
;         if (PROBE_MASK) { const unsigned long long t_ = __builtin_amdgcn_s_memrealtime(); if ((PROBE_MASK >> (k)) & 1u) pr_acc += t_ - pr_t0; pr_t0 = t_; } } while (0)
; __device__ __forceinline__ void convert_deferred(const Ptrs& P, unsigned char* lds, int quota) {
;     const int tid = threadIdx.x, wid = tid >> 6, lane = tid & 63;
;     float* tile = (float*)lds;
;     volatile __attribute__((address_space(3))) int* slot = (volatile __attribute__((address_space(3))) int*)((__attribute__((address_space(3))) unsigned char*)lds + 131072 + 320 + 11000);
;     unsigned* q = (unsigned*)(P.ws + WS_CTL) + CW_DEFQ;
;     for (int n = 0; n < quota; ++n) {
;         __syncthreads();
;         if (tid == 0) *slot = (int)atomicAdd(q, 1u);
;         __syncthreads();
;         const int t = *slot;
; __global__ void __launch_bounds__(NT, 2) mega(Args args) {
;     ...
;         if (IDLE_LAST(68 * 12)) convert_deferred(P, lds, 4); } SEAM(11);
.LBB0_1851:
	s_abs_i32 s0, s62
	v_cvt_f32_u32_e32 v2, s0
	s_sub_i32 s3, 0, s0
	v_readlane_b32 s56, v254, 40
	s_mov_b32 s1, 0
	v_rcp_iflag_f32_e32 v2, v2
	v_readlane_b32 s57, v254, 41
	v_mul_f32_e32 v2, 0x4f7ffffe, v2
	v_cvt_u32_f32_e32 v2, v2
	s_nop 0
	v_readfirstlane_b32 s4, v2
	s_mul_i32 s3, s3, s4
	s_mul_hi_u32 s3, s4, s3
	s_add_i32 s4, s4, s3
	s_mul_hi_u32 s3, s4, 0x330
	s_mul_i32 s3, s3, s0
	s_sub_i32 s3, 0x330, s3
	s_sub_i32 s4, s3, s0
	s_cmp_ge_u32 s3, s0
	s_cselect_b32 s3, s4, s3
	s_sub_i32 s4, s3, s0
	s_cmp_ge_u32 s3, s0
	s_cselect_b32 s0, s4, s3
	s_cmp_eq_u32 s0, 0
	s_cselect_b64 s[4:5], -1, 0
	s_cmp_lt_i32 s2, s0
	s_cselect_b64 s[6:7], -1, 0
	s_or_b64 s[4:5], s[4:5], s[6:7]
	s_and_b64 vcc, exec, s[4:5]
	s_cbranch_vccnz .LBB0_1861
	v_and_b32_e32 v2, 0x7c, v218
	v_lshlrev_b32_e32 v3, 5, v0
	s_movk_i32 s0, 0x400
	v_and_or_b32 v12, v3, s0, v2
	v_bfe_u32 v2, v0, 3, 3
	v_lshl_or_b32 v4, v1, 5, v2
	v_lshlrev_b32_e32 v2, 3, v0
	v_lshl_add_u32 v11, v182, 4, 0
	v_and_b32_e32 v2, 56, v2
	v_mul_u32_u24_e32 v16, 0x2020, v1
	v_mov_b32_e32 v3, 0
	s_waitcnt vmcnt(0)
	v_lshl_add_u32 v27, v4, 2, 0
	v_mul_u32_u24_e32 v28, 0x404, v2
	v_lshlrev_b32_e32 v10, 6, v4
	s_add_i32 s10, 0, 0x22c38
	v_add_u32_e32 v16, v11, v16
	v_and_b32_e32 v13, 0xfc, v218
	v_and_b32_e32 v14, 56, v179
	s_mov_b32 s3, 6
	v_or_b32_e32 v4, 0x200, v10
	v_mov_b32_e32 v5, v3
	v_or_b32_e32 v6, 0x400, v10
	v_mov_b32_e32 v7, v3
	v_or_b32_e32 v8, 0x600, v10
	v_mov_b32_e32 v9, v3
	v_mov_b32_e32 v15, s10
	s_movk_i32 s11, 0xb21
	s_movk_i32 s12, 0x800
	s_mov_b32 s13, 0x1104e000
	s_movk_i32 s14, 0x4de
	v_add_u32_e32 v17, 0x404, v16
	v_add_u32_e32 v18, 0x40c, v16
	v_add_u32_e32 v19, 0x808, v16
	v_add_u32_e32 v20, 0xc0c, v16
	v_add_u32_e32 v21, 0xc14, v16
	v_add_u32_e32 v22, 0x1414, v16
	v_add_u32_e32 v23, 0x141c, v16
	v_add_u32_e32 v24, 0x1818, v16
	v_add_u32_e32 v25, 0x1c1c, v16
	v_add_u32_e32 v26, 0x1c24, v16
	v_lshlrev_b32_e32 v2, 1, v2
	v_add_u32_e32 v27, v27, v28
	v_lshlrev_b32_e32 v10, 1, v10
	s_branch .LBB0_1854

; __device__ __forceinline__ unsigned g8_cvt_pk(float lo, float hi) { unsigned r; asm volatile("v_cvt_pk_bf16_f32 %0, %1, %2" : "=v"(r) : "v"(lo), "v"(hi)); return r; }
; __device__ __forceinline__ void convert_deferred(const Ptrs& P, unsigned char* lds, int quota) {
;     ...
;         __syncthreads();
;         if (tid == 0) *slot = (int)atomicAdd(q, 1u);
;         __syncthreads();
;         const int t = *slot;
;         if (t >= DEF_GU + DEF_DN) break;
;         const bool gu = t < DEF_GU;
;         const float* src = gu ? P.in[34] : P.in[36]; bf16* dst = (bf16*)(P.ws + (gu ? WS_WGU : WS_WDN));
;         const int N = gu ? 2048 : 1024, ntn = N / 256, it = gu ? 2 * NE * 16 * 8 - DEF_GU + t : 2 * NE * 16 * 4 - DEF_DN + (t - DEF_GU);
;         f32x4 cur[8];
;         bt_load(src, N, gu ? 1 : 0, it, ntn, cur);
; #pragma unroll
;         for (int i = 0; i < 8; ++i) { float* tp = tile + (wid * 8 + i) * 257 + lane * 4; tp[0] = cur[i][0]; tp[1] = cur[i][1]; tp[2] = cur[i][2]; tp[3] = cur[i][3]; }
;         __syncthreads();
;         const int per = 16 * ntn, z = it / per, r = it % per, kt = r / ntn, nt = r % ntn;
;         bf16* d = dst + (size_t)z * N * 1024 + (((size_t)nt * 16 + kt) << 14);
;         const int kc = lane & 7;
; #pragma unroll
;         for (int pss = 0; pss < 4; ++pss) {
;             const int nn = wid * 32 + pss * 8 + (lane >> 3); float f[8];
; #pragma unroll
;             for (int j = 0; j < 8; ++j) f[j] = tile[(kc * 8 + j) * 257 + nn];
;             u32x4 w; w.x = g8_cvt_pk(f[0], f[1]); w.y = g8_cvt_pk(f[2], f[3]); w.z = g8_cvt_pk(f[4], f[5]); w.w = g8_cvt_pk(f[6], f[7]);
;             *(u32x4*)(d + nn * 64 + kc * 8) = w;
;         }
.LBB0_1858:
	s_or_b64 exec, exec, s[4:5]
	s_waitcnt lgkmcnt(0)
	s_barrier
	ds_read_b32 v11, v15
	s_mov_b64 s[4:5], -1
	s_waitcnt lgkmcnt(0)
	v_cmp_lt_i32_e32 vcc, s11, v11
	v_readfirstlane_b32 s0, v11
	s_cbranch_vccnz .LBB0_1853
	s_cmpk_gt_i32 s0, 0x76b
	s_cselect_b64 vcc, -1, 0
	s_and_b64 s[4:5], vcc, exec
	s_cselect_b32 s4, s13, 0x104e000
	s_cselect_b32 s9, 0x400, s12
	s_cselect_b32 s15, s73, s69
	s_cselect_b32 s20, s72, s68
	s_cselect_b32 s5, s14, 0x1894
	s_cselect_b32 s16, 20, 21
	s_cselect_b32 s21, 10, 11
	s_add_u32 s22, s78, s4
	s_addc_u32 s23, s79, 0
	s_lshr_b32 s6, s9, 4
	s_abs_i32 s4, s6
	v_cvt_f32_u32_e32 v11, s4
	s_sub_i32 s17, 0, s4
	s_add_i32 s5, s5, s0
	s_abs_i32 s7, s5
	v_rcp_iflag_f32_e32 v11, v11
	s_xor_b32 s0, s5, s6
	s_lshr_b32 s8, s9, 8
	s_ashr_i32 s0, s0, 31
	v_mul_f32_e32 v11, 0x4f7ffffe, v11
	v_cvt_u32_f32_e32 v11, v11
	s_nop 0
	v_readfirstlane_b32 s24, v11
	s_mul_i32 s17, s17, s24
	s_mul_hi_u32 s17, s24, s17
	s_add_i32 s24, s24, s17
	s_mul_hi_u32 s17, s7, s24
	s_mul_i32 s24, s17, s4
	s_sub_i32 s7, s7, s24
	s_add_i32 s24, s17, 1
	s_sub_i32 s25, s7, s4
	s_cmp_ge_u32 s7, s4
	s_cselect_b32 s17, s24, s17
	s_cselect_b32 s7, s25, s7
	s_add_i32 s24, s17, 1
	s_cmp_ge_u32 s7, s4
	s_cselect_b32 s4, s24, s17
	s_xor_b32 s4, s4, s0
	s_sub_i32 s4, s4, s0
	s_sext_i32_i8 s0, s8
	v_cvt_f32_i32_e32 v11, s0
	s_mul_i32 s6, s4, s6
	s_sub_i32 s5, s5, s6
	v_cvt_f32_i32_e32 v28, s5
	v_rcp_iflag_f32_e32 v29, v11
	s_xor_b32 s0, s5, s0
	s_ashr_i32 s0, s0, 30
	s_or_b32 s0, s0, 1
	v_mul_f32_e32 v29, v28, v29
	v_trunc_f32_e32 v29, v29
	v_fma_f32 v28, -v29, v11, v28
	v_cvt_i32_f32_e32 v29, v29
	v_cmp_ge_f32_e64 s[6:7], |v28|, |v11|
	s_and_b64 s[6:7], s[6:7], exec
	s_cselect_b32 s0, s0, 0
	v_readfirstlane_b32 s6, v29
	s_add_i32 s6, s6, s0
	s_mul_i32 s7, s6, s8
	s_sub_i32 s8, s5, s7
	s_sext_i32_i8 s5, s8
	v_lshl_add_u32 v11, s5, 7, v12
	v_lshl_or_b32 v28, s5, 8, v13
	s_ashr_i32 s5, s4, 31
	s_sext_i32_i8 s0, s6
	s_lshl_b64 s[16:17], s[4:5], s16
	v_lshl_or_b32 v30, s0, 6, v14
	s_lshl_b64 s[16:17], s[16:17], 2
	v_ashrrev_i32_e32 v31, 31, v30
	s_add_u32 s16, s20, s16
	v_cndmask_b32_e32 v28, v11, v28, vcc
	s_addc_u32 s17, s15, s17
	v_lshlrev_b64 v[30:31], s21, v[30:31]
	v_lshl_add_u64 v[30:31], v[30:31], 2, s[16:17]
	v_ashrrev_i32_e32 v29, 31, v28
	v_lshl_add_u64 v[52:53], v[28:29], 2, v[30:31]
	s_lshl_b64 s[16:17], 12, s21
	s_lshl_b32 s0, s9, 2
	v_lshl_add_u64 v[40:41], v[52:53], 0, s[16:17]
	s_lshl_b64 s[16:17], 24, s21
	v_lshl_add_u64 v[36:37], v[52:53], 0, s[0:1]
	v_lshl_add_u64 v[44:45], v[52:53], 0, s[16:17]
	s_lshl_b64 s[16:17], 28, s21
	v_lshl_add_u64 v[54:55], v[36:37], 0, s[0:1]
	v_lshl_add_u64 v[48:49], v[52:53], 0, s[16:17]
	s_lshl_b32 s0, s9, 3
	s_lshl_b64 s[16:17], 20, s21
	global_load_dwordx4 v[28:31], v[52:53], off nt
	global_load_dwordx4 v[32:35], v[36:37], off nt
	s_nop 0
	global_load_dwordx4 v[36:39], v[54:55], off nt
	s_nop 0
	global_load_dwordx4 v[40:43], v[40:41], off nt
	v_lshl_add_u64 v[54:55], v[54:55], 0, s[0:1]
	v_lshl_add_u64 v[56:57], v[52:53], 0, s[16:17]
	global_load_dwordx4 v[44:47], v[44:45], off nt
	s_nop 0
	global_load_dwordx4 v[48:51], v[48:49], off nt
	s_nop 0
	global_load_dwordx4 v[52:55], v[54:55], off nt
	s_nop 0
	global_load_dwordx4 v[56:59], v[56:57], off nt
	s_lshl_b64 s[4:5], s[4:5], s21
	s_lshl_b64 s[4:5], s[4:5], 11
	s_add_u32 s0, s22, s4
	s_addc_u32 s9, s23, s5
	s_bfe_i64 s[4:5], s[8:9], 0x80000
	s_bfe_i64 s[6:7], s[6:7], 0x80000
	s_lshl_b64 s[4:5], s[4:5], 19
	s_add_u32 s0, s0, s4
	s_addc_u32 s8, s9, s5
	s_lshl_b64 s[4:5], s[6:7], 15
	s_add_u32 s4, s0, s4
	s_addc_u32 s5, s8, s5
	v_mov_b32_e32 v11, v3
	s_add_i32 s3, s3, -1
	s_cmp_eq_u32 s3, 0
	s_waitcnt vmcnt(7)
	ds_write_b128 v16, v[28:31]
	s_waitcnt vmcnt(6)
	ds_write2_b32 v17, v32, v33 offset1:1
	ds_write2_b32 v18, v34, v35 offset1:1
	s_waitcnt vmcnt(3)
	ds_write2_b64 v24, v[44:45], v[46:47] offset1:1
	s_waitcnt vmcnt(2)
	ds_write2_b32 v25, v48, v49 offset1:1
	ds_write2_b32 v26, v50, v51 offset1:1
	ds_write2_b64 v19, v[36:37], v[38:39] offset1:1
	ds_write2_b32 v20, v40, v41 offset1:1
	ds_write2_b32 v21, v42, v43 offset1:1
	s_waitcnt vmcnt(1)
	ds_write_b128 v16, v[52:55] offset:4112
	s_waitcnt vmcnt(0)
	ds_write2_b32 v22, v56, v57 offset1:1
	ds_write2_b32 v23, v58, v59 offset1:1
	s_waitcnt lgkmcnt(0)
	s_barrier
	ds_read_b32 v28, v27 offset:1028
	ds_read_b32 v29, v27 offset:3084
	ds_read_b32 v30, v27 offset:5140
	ds_read_b32 v31, v27 offset:7196
	ds_read_b32 v32, v27 offset:6168
	ds_read_b32 v33, v27 offset:4112
	ds_read_b32 v34, v27 offset:2056
	ds_read_b32 v35, v27
	s_waitcnt lgkmcnt(0)
	v_cvt_pk_bf16_f32 v28, v35, v28
	v_cvt_pk_bf16_f32 v29, v34, v29
	v_cvt_pk_bf16_f32 v30, v33, v30
	v_cvt_pk_bf16_f32 v31, v32, v31
	ds_read_b32 v36, v27 offset:1060
	ds_read_b32 v37, v27 offset:3116
	ds_read_b32 v38, v27 offset:5172
	ds_read_b32 v39, v27 offset:7228
	ds_read_b32 v40, v27 offset:6200
	ds_read_b32 v41, v27 offset:4144
	ds_read_b32 v42, v27 offset:2088
	ds_read_b32 v43, v27 offset:32
	v_lshl_add_u64 v[32:33], s[4:5], 0, v[2:3]
	v_lshl_add_u64 v[34:35], v[32:33], 0, v[10:11]
	global_store_dwordx4 v[34:35], v[28:31], off
	v_lshl_add_u64 v[34:35], v[4:5], 1, v[32:33]
	s_cselect_b64 s[4:5], -1, 0
	s_waitcnt lgkmcnt(0)
	v_cvt_pk_bf16_f32 v28, v43, v36
	v_cvt_pk_bf16_f32 v29, v42, v37
	v_cvt_pk_bf16_f32 v30, v41, v38
	v_cvt_pk_bf16_f32 v31, v40, v39
	ds_read_b32 v11, v27 offset:1092
	ds_read_b32 v36, v27 offset:3148
	ds_read_b32 v37, v27 offset:6232
	ds_read_b32 v38, v27 offset:4176
	ds_read_b32 v39, v27 offset:2120
	ds_read_b32 v40, v27 offset:64
	ds_read_b32 v41, v27 offset:5204
	ds_read_b32 v42, v27 offset:7260
	global_store_dwordx4 v[34:35], v[28:31], off
	v_lshl_add_u64 v[34:35], v[6:7], 1, v[32:33]
	v_lshl_add_u64 v[32:33], v[8:9], 1, v[32:33]
	s_waitcnt lgkmcnt(2)
	v_cvt_pk_bf16_f32 v28, v40, v11
	v_cvt_pk_bf16_f32 v29, v39, v36
	s_waitcnt lgkmcnt(1)
	v_cvt_pk_bf16_f32 v30, v38, v41
	s_waitcnt lgkmcnt(0)
	v_cvt_pk_bf16_f32 v31, v37, v42
	ds_read_b32 v11, v27 offset:1124
	ds_read_b32 v36, v27 offset:3180
	ds_read_b32 v37, v27 offset:6264
	ds_read_b32 v38, v27 offset:4208
	ds_read_b32 v39, v27 offset:2152
	ds_read_b32 v40, v27 offset:96
	ds_read_b32 v41, v27 offset:5236
	ds_read_b32 v42, v27 offset:7292
	global_store_dwordx4 v[34:35], v[28:31], off
	s_waitcnt lgkmcnt(2)
	s_nop 0
	v_cvt_pk_bf16_f32 v28, v40, v11
	v_cvt_pk_bf16_f32 v29, v39, v36
	s_waitcnt lgkmcnt(1)
	v_cvt_pk_bf16_f32 v30, v38, v41
	s_waitcnt lgkmcnt(0)
	v_cvt_pk_bf16_f32 v31, v37, v42
	global_store_dwordx4 v[32:33], v[28:31], off
	s_branch .LBB0_1853

; #define SEAM(k) do { if (IN(k) && IN((k) + 1)) xcd_barrier(bar); \
;         if (PROBE_MASK) { const unsigned long long t_ = __builtin_amdgcn_s_memrealtime(); if ((PROBE_MASK >> (k)) & 1u) pr_acc += t_ - pr_t0; pr_t0 = t_; } } while (0)
; __device__ __forceinline__ void convert_deferred(const Ptrs& P, unsigned char* lds, int quota) {
;     const int tid = threadIdx.x, wid = tid >> 6, lane = tid & 63;
;     float* tile = (float*)lds;
;     volatile __attribute__((address_space(3))) int* slot = (volatile __attribute__((address_space(3))) int*)((__attribute__((address_space(3))) unsigned char*)lds + 131072 + 320 + 11000);
;     unsigned* q = (unsigned*)(P.ws + WS_CTL) + CW_DEFQ;
;     for (int n = 0; n < quota; ++n) {
;         __syncthreads();
;         if (tid == 0) *slot = (int)atomicAdd(q, 1u);
;         __syncthreads();
;         const int t = *slot;
; __global__ void __launch_bounds__(NT, 2) mega(Args args) {
;     ...
;     if (IN(15)) { ph_norm2_router(P, lds, 1, 1); convert_deferred(P, lds, 1 << 20); } SEAM(15);
.LBB0_2278:
	v_and_b32_e32 v2, 0x7c, v179
	v_lshlrev_b32_e32 v3, 5, v0
	s_movk_i32 s0, 0x400
	v_and_or_b32 v12, v3, s0, v2
	v_lshrrev_b32_e32 v2, 3, v0
	v_and_b32_e32 v14, 56, v2
	v_lshrrev_b32_e32 v2, 3, v182
	v_lshl_or_b32 v4, v1, 5, v2
	v_lshl_add_u32 v5, v182, 4, 0
	v_and_b32_e32 v2, 56, v188
	v_lshl_add_u32 v7, v4, 2, 0
	v_mul_u32_u24_e32 v11, 0x2020, v1
	v_lshlrev_b32_e32 v4, 6, v4
	v_mul_u32_u24_e32 v9, 0x404, v2
	v_or_b32_e32 v6, 0x200, v4
	v_or_b32_e32 v8, 0x400, v4
	v_or_b32_e32 v10, 0x600, v4
	s_add_i32 s10, 0, 0x22c38
	v_add_u32_e32 v16, v5, v11
	v_and_b32_e32 v13, 0xfc, v179
	s_mov_b32 s1, 0
	v_mov_b32_e32 v3, 0
	s_mov_b32 s3, 0x100000
	v_mov_b32_e32 v15, s10
	s_movk_i32 s11, 0xb21
	s_movk_i32 s12, 0x800
	s_mov_b32 s13, 0x1104e000
	s_movk_i32 s14, 0x4de
	v_add_u32_e32 v17, 0x404, v16
	v_add_u32_e32 v18, 0x40c, v16
	v_add_u32_e32 v19, 0x808, v16
	v_add_u32_e32 v20, 0xc0c, v16
	v_add_u32_e32 v21, 0xc14, v16
	v_add_u32_e32 v22, 0x1414, v16
	v_add_u32_e32 v23, 0x141c, v16
	v_add_u32_e32 v24, 0x1818, v16
	v_add_u32_e32 v25, 0x1c1c, v16
	v_add_u32_e32 v26, 0x1c24, v16
	v_lshlrev_b32_e32 v2, 1, v2
	v_add_u32_e32 v27, v7, v9
	v_lshlrev_b32_e32 v4, 1, v4
	v_lshlrev_b32_e32 v6, 1, v6
	v_lshlrev_b32_e32 v8, 1, v8
	v_lshlrev_b32_e32 v10, 1, v10
	s_branch .LBB0_2280

; __device__ __forceinline__ unsigned g8_cvt_pk(float lo, float hi) { unsigned r; asm volatile("v_cvt_pk_bf16_f32 %0, %1, %2" : "=v"(r) : "v"(lo), "v"(hi)); return r; }
; __device__ __forceinline__ void convert_deferred(const Ptrs& P, unsigned char* lds, int quota) {
;     ...
;         __syncthreads();
;         if (tid == 0) *slot = (int)atomicAdd(q, 1u);
;         __syncthreads();
;         const int t = *slot;
;         if (t >= DEF_GU + DEF_DN) break;
;         const bool gu = t < DEF_GU;
;         const float* src = gu ? P.in[34] : P.in[36]; bf16* dst = (bf16*)(P.ws + (gu ? WS_WGU : WS_WDN));
;         const int N = gu ? 2048 : 1024, ntn = N / 256, it = gu ? 2 * NE * 16 * 8 - DEF_GU + t : 2 * NE * 16 * 4 - DEF_DN + (t - DEF_GU);
;         f32x4 cur[8];
;         bt_load(src, N, gu ? 1 : 0, it, ntn, cur);
; #pragma unroll
;         for (int i = 0; i < 8; ++i) { float* tp = tile + (wid * 8 + i) * 257 + lane * 4; tp[0] = cur[i][0]; tp[1] = cur[i][1]; tp[2] = cur[i][2]; tp[3] = cur[i][3]; }
;         __syncthreads();
;         const int per = 16 * ntn, z = it / per, r = it % per, kt = r / ntn, nt = r % ntn;
;         bf16* d = dst + (size_t)z * N * 1024 + (((size_t)nt * 16 + kt) << 14);
;         const int kc = lane & 7;
; #pragma unroll
;         for (int pss = 0; pss < 4; ++pss) {
;             const int nn = wid * 32 + pss * 8 + (lane >> 3); float f[8];
; #pragma unroll
;             for (int j = 0; j < 8; ++j) f[j] = tile[(kc * 8 + j) * 257 + nn];
;             u32x4 w; w.x = g8_cvt_pk(f[0], f[1]); w.y = g8_cvt_pk(f[2], f[3]); w.z = g8_cvt_pk(f[4], f[5]); w.w = g8_cvt_pk(f[6], f[7]);
;             *(u32x4*)(d + nn * 64 + kc * 8) = w;
;         }
.LBB0_2284:
	s_or_b64 exec, exec, s[4:5]
	s_waitcnt lgkmcnt(0)
	s_barrier
	ds_read_b32 v5, v15
	s_mov_b64 s[4:5], -1
	s_waitcnt lgkmcnt(0)
	v_cmp_lt_i32_e32 vcc, s11, v5
	v_readfirstlane_b32 s0, v5
	s_cbranch_vccnz .LBB0_2279
	s_cmpk_gt_i32 s0, 0x76b
	s_cselect_b64 vcc, -1, 0
	s_and_b64 s[4:5], vcc, exec
	s_cselect_b32 s4, s13, 0x104e000
	s_cselect_b32 s9, 0x400, s12
	s_cselect_b32 s15, s73, s69
	s_cselect_b32 s18, s72, s68
	s_cselect_b32 s5, s14, 0x1894
	s_cselect_b32 s16, 20, 21
	s_cselect_b32 s19, 10, 11
	s_add_u32 s22, s78, s4
	s_addc_u32 s23, s79, 0
	s_lshr_b32 s6, s9, 4
	s_abs_i32 s4, s6
	v_cvt_f32_u32_e32 v5, s4
	s_sub_i32 s17, 0, s4
	s_add_i32 s5, s5, s0
	s_abs_i32 s7, s5
	v_rcp_iflag_f32_e32 v5, v5
	s_xor_b32 s0, s5, s6
	s_lshr_b32 s8, s9, 8
	s_ashr_i32 s0, s0, 31
	v_mul_f32_e32 v5, 0x4f7ffffe, v5
	v_cvt_u32_f32_e32 v5, v5
	s_nop 0
	v_readfirstlane_b32 s24, v5
	s_mul_i32 s17, s17, s24
	s_mul_hi_u32 s17, s24, s17
	s_add_i32 s24, s24, s17
	s_mul_hi_u32 s17, s7, s24
	s_mul_i32 s24, s17, s4
	s_sub_i32 s7, s7, s24
	s_add_i32 s24, s17, 1
	s_sub_i32 s25, s7, s4
	s_cmp_ge_u32 s7, s4
	s_cselect_b32 s17, s24, s17
	s_cselect_b32 s7, s25, s7
	s_add_i32 s24, s17, 1
	s_cmp_ge_u32 s7, s4
	s_cselect_b32 s4, s24, s17
	s_xor_b32 s4, s4, s0
	s_sub_i32 s4, s4, s0
	s_sext_i32_i8 s0, s8
	v_cvt_f32_i32_e32 v5, s0
	s_mul_i32 s6, s4, s6
	s_sub_i32 s5, s5, s6
	v_cvt_f32_i32_e32 v7, s5
	v_rcp_iflag_f32_e32 v9, v5
	s_xor_b32 s0, s5, s0
	s_ashr_i32 s0, s0, 30
	s_or_b32 s0, s0, 1
	v_mul_f32_e32 v9, v7, v9
	v_trunc_f32_e32 v9, v9
	v_fma_f32 v7, -v9, v5, v7
	v_cvt_i32_f32_e32 v9, v9
	v_cmp_ge_f32_e64 s[6:7], |v7|, |v5|
	s_and_b64 s[6:7], s[6:7], exec
	s_cselect_b32 s0, s0, 0
	v_readfirstlane_b32 s6, v9
	s_add_i32 s6, s6, s0
	s_mul_i32 s7, s6, s8
	s_sub_i32 s8, s5, s7
	s_sext_i32_i8 s5, s8
	v_lshl_add_u32 v5, s5, 7, v12
	v_lshl_or_b32 v7, s5, 8, v13
	s_ashr_i32 s5, s4, 31
	s_sext_i32_i8 s0, s6
	s_lshl_b64 s[16:17], s[4:5], s16
	v_lshl_or_b32 v30, s0, 6, v14
	s_lshl_b64 s[16:17], s[16:17], 2
	v_ashrrev_i32_e32 v31, 31, v30
	s_add_u32 s16, s18, s16
	v_cndmask_b32_e32 v28, v5, v7, vcc
	s_addc_u32 s17, s15, s17
	v_lshlrev_b64 v[30:31], s19, v[30:31]
	v_lshl_add_u64 v[30:31], v[30:31], 2, s[16:17]
	v_ashrrev_i32_e32 v29, 31, v28
	v_lshl_add_u64 v[52:53], v[28:29], 2, v[30:31]
	s_lshl_b32 s0, s9, 2
	s_lshl_b64 s[16:17], 12, s19
	v_lshl_add_u64 v[36:37], v[52:53], 0, s[0:1]
	v_lshl_add_u64 v[44:45], v[52:53], 0, s[16:17]
	s_lshl_b64 s[16:17], 24, s19
	v_lshl_add_u64 v[54:55], v[36:37], 0, s[0:1]
	v_lshl_add_u64 v[56:57], v[52:53], 0, s[16:17]
	s_lshl_b64 s[16:17], 28, s19
	s_lshl_b32 s0, s9, 3
	v_lshl_add_u64 v[58:59], v[52:53], 0, s[16:17]
	v_lshl_add_u64 v[60:61], v[54:55], 0, s[0:1]
	s_lshl_b64 s[16:17], 20, s19
	global_load_dwordx4 v[28:31], v[52:53], off nt
	global_load_dwordx4 v[32:35], v[36:37], off nt
	s_nop 0
	global_load_dwordx4 v[36:39], v[54:55], off nt
	global_load_dwordx4 v[40:43], v[44:45], off nt
	s_nop 0
	global_load_dwordx4 v[44:47], v[56:57], off nt
	global_load_dwordx4 v[48:51], v[58:59], off nt
	v_lshl_add_u64 v[62:63], v[52:53], 0, s[16:17]
	global_load_dwordx4 v[52:55], v[60:61], off nt
	global_load_dwordx4 v[56:59], v[62:63], off nt
	s_lshl_b64 s[4:5], s[4:5], s19
	s_lshl_b64 s[4:5], s[4:5], 11
	s_add_u32 s0, s22, s4
	s_addc_u32 s9, s23, s5
	s_bfe_i64 s[4:5], s[8:9], 0x80000
	s_bfe_i64 s[6:7], s[6:7], 0x80000
	s_lshl_b64 s[4:5], s[4:5], 19
	s_add_u32 s0, s0, s4
	s_addc_u32 s8, s9, s5
	s_lshl_b64 s[4:5], s[6:7], 15
	s_add_u32 s4, s0, s4
	s_addc_u32 s5, s8, s5
	v_mov_b32_e32 v5, v3
	s_add_i32 s3, s3, -1
	s_cmp_eq_u32 s3, 0
	s_waitcnt vmcnt(7)
	ds_write_b128 v16, v[28:31]
	s_waitcnt vmcnt(6)
	ds_write2_b32 v17, v32, v33 offset1:1
	ds_write2_b32 v18, v34, v35 offset1:1
	s_waitcnt vmcnt(3)
	ds_write2_b64 v24, v[44:45], v[46:47] offset1:1
	s_waitcnt vmcnt(2)
	ds_write2_b32 v25, v48, v49 offset1:1
	ds_write2_b32 v26, v50, v51 offset1:1
	ds_write2_b64 v19, v[36:37], v[38:39] offset1:1
	ds_write2_b32 v20, v40, v41 offset1:1
	ds_write2_b32 v21, v42, v43 offset1:1
	s_waitcnt vmcnt(1)
	ds_write_b128 v16, v[52:55] offset:4112
	s_waitcnt vmcnt(0)
	ds_write2_b32 v22, v56, v57 offset1:1
	ds_write2_b32 v23, v58, v59 offset1:1
	s_waitcnt lgkmcnt(0)
	s_barrier
	ds_read_b32 v7, v27 offset:1028
	ds_read_b32 v9, v27 offset:3084
	ds_read_b32 v11, v27 offset:5140
	ds_read_b32 v31, v27 offset:7196
	ds_read_b32 v32, v27 offset:6168
	ds_read_b32 v30, v27 offset:4112
	ds_read_b32 v29, v27 offset:2056
	ds_read_b32 v28, v27
	s_waitcnt lgkmcnt(0)
	v_cvt_pk_bf16_f32 v28, v28, v7
	v_cvt_pk_bf16_f32 v29, v29, v9
	v_cvt_pk_bf16_f32 v30, v30, v11
	v_cvt_pk_bf16_f32 v31, v32, v31
	ds_read_b32 v7, v27 offset:1060
	ds_read_b32 v9, v27 offset:3116
	ds_read_b32 v11, v27 offset:5172
	ds_read_b32 v36, v27 offset:7228
	ds_read_b32 v37, v27 offset:6200
	ds_read_b32 v38, v27 offset:4144
	ds_read_b32 v39, v27 offset:2088
	ds_read_b32 v40, v27 offset:32
	v_lshl_add_u64 v[32:33], s[4:5], 0, v[2:3]
	v_lshl_add_u64 v[34:35], v[32:33], 0, v[4:5]
	global_store_dwordx4 v[34:35], v[28:31], off
	s_cselect_b64 s[4:5], -1, 0
	s_waitcnt lgkmcnt(0)
	v_cvt_pk_bf16_f32 v28, v40, v7
	v_cvt_pk_bf16_f32 v29, v39, v9
	v_cvt_pk_bf16_f32 v30, v38, v11
	v_cvt_pk_bf16_f32 v31, v37, v36
	ds_read_b32 v5, v27 offset:1092
	ds_read_b32 v9, v27 offset:3148
	ds_read_b32 v11, v27 offset:5204
	ds_read_b32 v36, v27 offset:6232
	ds_read_b32 v37, v27 offset:4176
	ds_read_b32 v38, v27 offset:2120
	ds_read_b32 v39, v27 offset:64
	ds_read_b32 v40, v27 offset:7260
	v_mov_b32_e32 v7, v3
	v_lshl_add_u64 v[34:35], v[32:33], 0, v[6:7]
	global_store_dwordx4 v[34:35], v[28:31], off
	s_waitcnt lgkmcnt(1)
	s_nop 0
	v_cvt_pk_bf16_f32 v28, v39, v5
	v_cvt_pk_bf16_f32 v29, v38, v9
	v_cvt_pk_bf16_f32 v30, v37, v11
	s_waitcnt lgkmcnt(0)
	v_cvt_pk_bf16_f32 v31, v36, v40
	ds_read_b32 v5, v27 offset:1124
	ds_read_b32 v7, v27 offset:3180
	ds_read_b32 v11, v27 offset:5236
	ds_read_b32 v36, v27 offset:6264
	ds_read_b32 v37, v27 offset:4208
	ds_read_b32 v38, v27 offset:2152
	ds_read_b32 v39, v27 offset:96
	ds_read_b32 v40, v27 offset:7292
	v_mov_b32_e32 v9, v3
	v_lshl_add_u64 v[34:35], v[32:33], 0, v[8:9]
	global_store_dwordx4 v[34:35], v[28:31], off
	s_waitcnt lgkmcnt(1)
	s_nop 0
	v_cvt_pk_bf16_f32 v28, v39, v5
	v_cvt_pk_bf16_f32 v29, v38, v7
	v_cvt_pk_bf16_f32 v30, v37, v11
	v_mov_b32_e32 v11, v3
	v_lshl_add_u64 v[32:33], v[32:33], 0, v[10:11]
	s_waitcnt lgkmcnt(0)
	v_cvt_pk_bf16_f32 v31, v36, v40
	global_store_dwordx4 v[32:33], v[28:31], off
	s_branch .LBB0_2279
